# v38 + lever 7 in P3: differential-attention sub-LN epilogue (16 serial 5-hop bpermute chains) via DPP + permlane16_swap
# baseline (speedup 1.0000x reference)
; #define LAS __attribute__((address_space(3)))
; __device__ __forceinline__ void finishSM(f32x16& p0, f32x16& p1, float alpha, float& l_reg, bf16x8& pa0, bf16x8& pa1, bf16x8& pa2, bf16x8& pa3) {
;     ...
;     for (int r = 0; r < 16; ++r) p1[r] = __builtin_amdgcn_exp2f(p1[r]);
;     float ps = 0;
; #pragma unroll
;     for (int r = 0; r < 16; ++r) ps += p0[r];
; #pragma unroll
;     for (int r = 0; r < 16; ++r) ps += p1[r];
;     { auto rr = __builtin_amdgcn_permlane32_swap(__float_as_uint(ps), __float_as_uint(ps), false, false);
;       ps = __uint_as_float(rr[0]) + __uint_as_float(rr[1]); }
;     l_reg = l_reg * alpha + ps;
;     ...
;     PK4(p0, 0, pa0); PK4(p0, 8, pa1); PK4(p1, 0, pa2); PK4(p1, 8, pa3);
;     ...
; }
; template <int MODE>
; __device__ __forceinline__ void qkt(f32x16& p0, f32x16& p1, const LAS unsigned char* Ks, const bf16x8* qr, const LAS unsigned char* Qs, int r32, int hi, int cbase) {
;     p0 = f32x16{}; p1 = f32x16{};
; #pragma unroll
;     for (int d0 = 0; d0 < Cfg<MODE>::ND; ++d0) { const int cb = cbase + (d0 * 16 + hi * 8) * 2;
;         const bf16x8 b0 = *(const LAS bf16x8*)(Ks + KSWZ(r32, cb));
;         const bf16x8 b1 = *(const LAS bf16x8*)(Ks + KSWZ(32 + r32, cb));
;         bf16x8 q; if constexpr (MODE == 0) q = *(const LAS bf16x8*)(Qs + KSWZ(r32, cb)); else q = qr[d0];
;         p0 = __builtin_amdgcn_mfma_f32_32x32x16_bf16(b0, q, p0, 0, 0, 0);
;         p1 = __builtin_amdgcn_mfma_f32_32x32x16_bf16(b1, q, p1, 0, 0, 0); }
; }
; __device__ __forceinline__ int v_st(int k, int c) { const int kk = (k & ~0xC) | ((k & 4) << 1) | ((k & 8) >> 1); return ((kk >> 3) * 4 + (c >> 5)) * 512 + ((kk & 7) * 32 + (c & 31)) * 2; }
; __device__ __forceinline__ int v_rd_base(int lane) { return ((lane & 3) << 3) | (((lane >> 2) & 3) << 6) | (((lane >> 4) & 1) << 5) | (((lane >> 5) & 1) << 8); }
; template <int OFF> __device__ __forceinline__ s16x4 tr_read(int vb) {
;     s16x4 r; asm volatile("ds_read_b64_tr_b16 %0, %1 offset:%2" : "=&v"(r) : "v"(vb), "i"(OFF) : "memory"); return r;
; }
; template <int D0> __device__ __forceinline__ void pv_one(f32x16& od, int vb, bf16x8 pa0, bf16x8 pa1, bf16x8 pa2, bf16x8 pa3) {
;     const s16x4 l0 = tr_read<v_rd_off(D0, 0, 0)>(vb), h0 = tr_read<v_rd_off(D0, 0, 1)>(vb), l1 = tr_read<v_rd_off(D0, 1, 0)>(vb), h1 = tr_read<v_rd_off(D0, 1, 1)>(vb);
.LBB0_447:
	v_exp_f32_e32 v102, v82
	v_exp_f32_e32 v103, v83
	v_exp_f32_e32 v82, v84
	v_fmamk_f32 v66, v66, 0x3e38aa3b, v101
	v_exp_f32_e32 v84, v85
	v_fmamk_f32 v113, v77, 0x3e38aa3b, v101
	v_exp_f32_e32 v77, v86
	v_exp_f32_e32 v85, v66
	v_add_f32_e32 v66, 0, v102
	v_exp_f32_e32 v83, v87
	v_add_f32_e32 v66, v103, v66
	v_fmamk_f32 v112, v76, 0x3e38aa3b, v101
	v_exp_f32_e32 v76, v88
	v_add_f32_e32 v66, v82, v66
	v_fmamk_f32 v114, v78, 0x3e38aa3b, v101
	v_exp_f32_e32 v78, v89
	v_add_f32_e32 v66, v84, v66
	v_fmamk_f32 v109, v73, 0x3e38aa3b, v101
	v_exp_f32_e32 v73, v90
	v_add_f32_e32 v66, v77, v66
	v_fmamk_f32 v111, v75, 0x3e38aa3b, v101
	v_exp_f32_e32 v75, v91
	v_add_f32_e32 v66, v83, v66
	v_fmamk_f32 v107, v71, 0x3e38aa3b, v101
	v_exp_f32_e32 v71, v92
	v_add_f32_e32 v66, v76, v66
	v_fmamk_f32 v110, v74, 0x3e38aa3b, v101
	v_exp_f32_e32 v74, v93
	v_add_f32_e32 v66, v78, v66
	v_fmamk_f32 v105, v69, 0x3e38aa3b, v101
	v_exp_f32_e32 v69, v94
	v_add_f32_e32 v66, v73, v66
	v_fmamk_f32 v108, v72, 0x3e38aa3b, v101
	v_exp_f32_e32 v72, v95
	v_add_f32_e32 v66, v75, v66
	v_fmamk_f32 v104, v68, 0x3e38aa3b, v101
	v_exp_f32_e32 v68, v96
	v_add_f32_e32 v66, v71, v66
	v_fmamk_f32 v106, v70, 0x3e38aa3b, v101
	v_exp_f32_e32 v70, v97
	v_add_f32_e32 v66, v74, v66
	v_fmamk_f32 v67, v67, 0x3e38aa3b, v101
	v_add_f32_e32 v66, v69, v66
	v_exp_f32_e32 v86, v67
	v_add_f32_e32 v66, v72, v66
	v_exp_f32_e32 v87, v104
	v_add_f32_e32 v66, v68, v66
	v_exp_f32_e32 v88, v105
	v_add_f32_e32 v66, v70, v66
	v_exp_f32_e32 v89, v106
	v_add_f32_e32 v66, v85, v66
	v_exp_f32_e32 v90, v107
	v_add_f32_e32 v66, v86, v66
	v_exp_f32_e32 v91, v108
	v_add_f32_e32 v66, v87, v66
	v_exp_f32_e32 v92, v109
	v_add_f32_e32 v66, v88, v66
	v_exp_f32_e32 v93, v110
	v_add_f32_e32 v66, v89, v66
	v_exp_f32_e32 v94, v111
	v_add_f32_e32 v66, v90, v66
	v_exp_f32_e32 v95, v112
	v_add_f32_e32 v66, v91, v66
	v_exp_f32_e32 v96, v113
	v_add_f32_e32 v66, v92, v66
	v_fmamk_f32 v79, v79, 0x3e38aa3b, v101
	v_exp_f32_e32 v97, v114
	v_add_f32_e32 v66, v93, v66
	v_fmamk_f32 v80, v80, 0x3e38aa3b, v101
	v_exp_f32_e32 v104, v79
	v_add_f32_e32 v66, v94, v66
	v_fmac_f32_e32 v101, 0x3e38aa3b, v81
	v_exp_f32_e32 v105, v80
	v_add_f32_e32 v66, v95, v66
	v_exp_f32_e32 v101, v101
	v_add_f32_e32 v66, v96, v66
	v_add_f32_e32 v66, v97, v66
	v_add_f32_e32 v66, v104, v66
	v_add_f32_e32 v66, v105, v66
	v_add_f32_e32 v66, v101, v66
	v_mov_b32_e32 v67, v66
	s_nop 1
	v_permlane32_swap_b32_e32 v66, v67
	v_cvt_pk_bf16_f32 v80, v102, v103
	v_cvt_pk_bf16_f32 v81, v82, v84
	v_cvt_pk_bf16_f32 v82, v77, v83
	v_cvt_pk_bf16_f32 v83, v76, v78
	v_cvt_pk_bf16_f32 v76, v73, v75
	v_cvt_pk_bf16_f32 v77, v71, v74
	v_cvt_pk_bf16_f32 v78, v69, v72
	v_cvt_pk_bf16_f32 v79, v68, v70
	v_cvt_pk_bf16_f32 v68, v85, v86
	v_cvt_pk_bf16_f32 v69, v87, v88
	v_cvt_pk_bf16_f32 v70, v89, v90
	v_cvt_pk_bf16_f32 v71, v91, v92
	v_cvt_pk_bf16_f32 v72, v93, v94
	v_cvt_pk_bf16_f32 v73, v95, v96
	v_cvt_pk_bf16_f32 v74, v97, v104
	v_cvt_pk_bf16_f32 v75, v105, v101
	s_nop 0
	v_permlane32_swap_b32_e32 v80, v82
	v_permlane32_swap_b32_e32 v81, v83
	v_permlane32_swap_b32_e32 v76, v78
	v_permlane32_swap_b32_e32 v77, v79
	v_permlane32_swap_b32_e32 v68, v70
	v_permlane32_swap_b32_e32 v69, v71
	v_permlane32_swap_b32_e32 v72, v74
	v_permlane32_swap_b32_e32 v73, v75
	ds_read_b64_tr_b16 v[84:85], v173 offset:0
	ds_read_b64_tr_b16 v[86:87], v173 offset:0x800
	ds_read_b64_tr_b16 v[88:89], v173 offset:0x1000
	ds_read_b64_tr_b16 v[90:91], v173 offset:0x1800
	ds_read_b64_tr_b16 v[92:93], v173 offset:0x2000
	ds_read_b64_tr_b16 v[94:95], v173 offset:0x2800
	ds_read_b64_tr_b16 v[102:103], v173 offset:0x3000
	ds_read_b64_tr_b16 v[104:105], v173 offset:0x3800
	s_waitcnt lgkmcnt(0)
	s_nop 0
	v_mfma_f32_32x32x16_bf16 v[2:17], v[80:83], v[84:87], v[2:17]
	ds_read_b64_tr_b16 v[84:85], v173 offset:0x200
	ds_read_b64_tr_b16 v[86:87], v173 offset:0xa00
	v_mfma_f32_32x32x16_bf16 v[2:17], v[76:79], v[88:91], v[2:17]
	ds_read_b64_tr_b16 v[88:89], v173 offset:0x1200
	ds_read_b64_tr_b16 v[90:91], v173 offset:0x1a00
	v_mfma_f32_32x32x16_bf16 v[2:17], v[68:71], v[92:95], v[2:17]
	ds_read_b64_tr_b16 v[92:93], v173 offset:0x2200
	ds_read_b64_tr_b16 v[94:95], v173 offset:0x2a00
	ds_read_b64_tr_b16 v[106:107], v173 offset:0x3200
	ds_read_b64_tr_b16 v[108:109], v173 offset:0x3a00
	v_mfma_f32_32x32x16_bf16 v[2:17], v[72:75], v[102:105], v[2:17]
	s_waitcnt lgkmcnt(0)
	v_mfma_f32_32x32x16_bf16 v[50:65], v[80:83], v[84:87], v[50:65]
	ds_read_b64_tr_b16 v[84:85], v173 offset:0x400
	ds_read_b64_tr_b16 v[86:87], v173 offset:0xc00
	v_mfma_f32_32x32x16_bf16 v[50:65], v[76:79], v[88:91], v[50:65]
	ds_read_b64_tr_b16 v[88:89], v173 offset:0x1400
	ds_read_b64_tr_b16 v[90:91], v173 offset:0x1c00
	v_mfma_f32_32x32x16_bf16 v[50:65], v[68:71], v[92:95], v[50:65]
	ds_read_b64_tr_b16 v[92:93], v173 offset:0x2400
	ds_read_b64_tr_b16 v[94:95], v173 offset:0x2c00
	ds_read_b64_tr_b16 v[102:103], v173 offset:0x3400
	ds_read_b64_tr_b16 v[104:105], v173 offset:0x3c00
	v_mfma_f32_32x32x16_bf16 v[50:65], v[72:75], v[106:109], v[50:65]
	s_waitcnt lgkmcnt(0)
	v_mfma_f32_32x32x16_bf16 v[34:49], v[80:83], v[84:87], v[34:49]
	ds_read_b64_tr_b16 v[84:85], v173 offset:0x600
	ds_read_b64_tr_b16 v[86:87], v173 offset:0xe00
	v_mfma_f32_32x32x16_bf16 v[34:49], v[76:79], v[88:91], v[34:49]
	ds_read_b64_tr_b16 v[88:89], v173 offset:0x1600
	ds_read_b64_tr_b16 v[90:91], v173 offset:0x1e00
	v_mfma_f32_32x32x16_bf16 v[34:49], v[68:71], v[92:95], v[34:49]
	ds_read_b64_tr_b16 v[92:93], v173 offset:0x2600
	ds_read_b64_tr_b16 v[94:95], v173 offset:0x2e00
	ds_read_b64_tr_b16 v[106:107], v173 offset:0x3600
	ds_read_b64_tr_b16 v[108:109], v173 offset:0x3e00
	v_mfma_f32_32x32x16_bf16 v[34:49], v[72:75], v[102:105], v[34:49]
	s_waitcnt lgkmcnt(0)
	v_mfma_f32_32x32x16_bf16 v[18:33], v[80:83], v[84:87], v[18:33]
	v_mfma_f32_32x32x16_bf16 v[18:33], v[76:79], v[88:91], v[18:33]
	v_mfma_f32_32x32x16_bf16 v[18:33], v[68:71], v[92:95], v[18:33]
	v_mfma_f32_32x32x16_bf16 v[18:33], v[72:75], v[106:109], v[18:33]
	s_and_saveexec_b64 s[4:5], s[0:1]
	v_add_f32_e32 v68, v98, v99
	v_fmac_f32_e32 v68, v178, v141
	v_add_f32_e32 v66, v66, v67
	v_fmac_f32_e32 v66, v68, v100
	ds_write_b32 v171, v66
	s_or_b64 exec, exec, s[4:5]
	s_waitcnt lgkmcnt(0)
	ds_read_b128 v[66:69], v207
	ds_read_b128 v[70:73], v207 offset:32
	ds_read_b128 v[104:107], v207 offset:64
	ds_read_b128 v[108:111], v207 offset:96
	s_waitcnt lgkmcnt(0)
	s_barrier
; __device__ __forceinline__ unsigned cvt_pk_bf16(float lo, float hi) { unsigned r; asm volatile("v_cvt_pk_bf16_f32 %0, %1, %2" : "=v"(r) : "v"(lo), "v"(hi)); return r; }
; __device__ __forceinline__ float bf_lo(unsigned w) { return __uint_as_float(w << 16); }
; __device__ __forceinline__ float bf_hi(unsigned w) { return __uint_as_float(w & 0xffff0000u); }
; __device__ __forceinline__ int crow(int r, int hi) { return (r & 3) + 8 * (r >> 2) + 4 * hi; }
; template <int MODE>
; __device__ __forceinline__ void attn_pass(const bf16_t* __restrict__ Qb, const bf16_t* __restrict__ Kh, const bf16_t* __restrict__ Vh, const int NT, const int kr0, const int g4, const int map,
;                                           LAS unsigned char* lds, f32x16 (&o)[4]) {
;     ...
;     for (int r = 0; r < 16; ++r) { const float rl = __builtin_amdgcn_rcpf(li_l[crow(r, hi)]);
; #pragma unroll
;         for (int d = 0; d < 4; ++d) o[d][r] *= rl; }
; __device__ __forceinline__ void p3_attention(Frame& F) {
;     ...
;         for (int k = 0; k < 8; ++k) { const int d = k >> 1, r0 = (k & 1) * 8; u32x4 w;
;             w.x = cvt_pk_bf16(o[d][r0], o[d][r0 + 1]); w.y = cvt_pk_bf16(o[d][r0 + 2], o[d][r0 + 3]); w.z = cvt_pk_bf16(o[d][r0 + 4], o[d][r0 + 5]); w.w = cvt_pk_bf16(o[d][r0 + 6], o[d][r0 + 7]);
;             o1l[k * 512] = w; }
;         attn::attn_pass<1>(Qb + 64, Kh, Vh, RPB / 64, 0, 0, 1, F.lds, o);
;         float sw[4];
; #pragma unroll
;         for (int d = 0; d < 4; ++d) sw[d] = F.in[I_SUBLN][d * 32 + r32] * (1.0f - LAM_INIT);
;         u32x4 o1p[8];
; #pragma unroll
;         for (int k = 0; k < 8; ++k) o1p[k] = o1l[k * 512];
;         int hi1 = hi, r32a = r32; asm volatile("" : "+v"(hi1), "+v"(r32a));
;         unsigned char* od = F.ws + WS_ODF + (size_t)(b * SEQ + qb * 256 + wid * 32) * 1024 + h * 128 + r32a;
; #pragma unroll
;         for (int r = 0; r < 16; ++r) {
;             float dd[4], ss = 0.f;
; #pragma unroll
;             for (int d = 0; d < 4; ++d) { const unsigned pw = o1p[d * 2 + (r >> 3)][(r & 7) >> 1]; const float o1 = (r & 1) ? bf_hi(pw) : bf_lo(pw); dd[d] = o1 - lam * o[d][r]; ss += dd[d] * dd[d]; }
;             ss += __shfl_xor(ss, 1); ss += __shfl_xor(ss, 2); ss += __shfl_xor(ss, 4); ss += __shfl_xor(ss, 8); ss += __shfl_xor(ss, 16);
;             const float rs = 1.0f / sqrtf(ss * (1.0f / 128.0f) + RMS_EPS);
	v_rcp_f32_e32 v75, v66
	v_rcp_f32_e32 v67, v67
	v_sub_f32_e32 v74, v199, v177
	v_mul_f32_e32 v103, v2, v75
	v_lshlrev_b32_e32 v2, 2, v172
	v_mul_f32_e32 v112, v50, v75
	global_load_dword v50, v2, s[60:61]
	global_load_dword v113, v2, s[60:61] offset:128
	global_load_dword v114, v2, s[60:61] offset:256
	s_nop 0
	global_load_dword v2, v2, s[60:61] offset:384
	v_mul_f32_e32 v117, v3, v67
	v_rcp_f32_e32 v3, v68
	v_mul_f32_e32 v115, v34, v75
	v_mul_f32_e32 v116, v18, v75
	v_add_f32_e32 v66, 0x3e4ccccd, v74
	v_mul_f32_e32 v121, v4, v3
	v_rcp_f32_e32 v4, v69
	v_mul_f32_e32 v122, v52, v3
	v_mul_f32_e32 v123, v36, v3
	v_mul_f32_e32 v124, v20, v3
	v_rcp_f32_e32 v3, v70
	v_mul_f32_e32 v125, v5, v4
	v_mul_f32_e32 v126, v53, v4
	v_mul_f32_e32 v127, v37, v4
	v_mul_f32_e32 v128, v21, v4
	v_rcp_f32_e32 v4, v71
	v_mul_f32_e32 v101, v6, v3
	v_mul_f32_e32 v102, v54, v3
	v_mul_f32_e32 v100, v38, v3
	v_mul_f32_e32 v99, v22, v3
	v_rcp_f32_e32 v3, v72
	v_mul_f32_e32 v97, v7, v4
	v_mul_f32_e32 v98, v55, v4
	v_mul_f32_e32 v96, v39, v4
	v_mul_f32_e32 v95, v23, v4
	v_rcp_f32_e32 v4, v73
	v_mul_f32_e32 v93, v8, v3
	v_mul_f32_e32 v94, v56, v3
	v_mul_f32_e32 v92, v40, v3
	v_mul_f32_e32 v91, v24, v3
	v_rcp_f32_e32 v3, v104
	v_mul_f32_e32 v89, v9, v4
	v_mul_f32_e32 v90, v57, v4
	v_mul_f32_e32 v88, v41, v4
	v_mul_f32_e32 v87, v25, v4
	v_rcp_f32_e32 v4, v105
	v_mul_f32_e32 v85, v10, v3
	v_mul_f32_e32 v86, v58, v3
	v_mul_f32_e32 v84, v42, v3
	v_mul_f32_e32 v83, v26, v3
	v_rcp_f32_e32 v3, v106
	v_mul_f32_e32 v81, v11, v4
	v_mul_f32_e32 v82, v59, v4
	v_mul_f32_e32 v80, v43, v4
	v_mul_f32_e32 v79, v27, v4
	v_rcp_f32_e32 v4, v107
	v_mul_f32_e32 v77, v12, v3
	v_mul_f32_e32 v78, v60, v3
	v_mul_f32_e32 v76, v44, v3
	v_mul_f32_e32 v75, v28, v3
	v_rcp_f32_e32 v3, v108
	v_mul_f32_e32 v73, v13, v4
	v_mul_f32_e32 v74, v61, v4
	v_mul_f32_e32 v72, v45, v4
	v_mul_f32_e32 v71, v29, v4
	v_rcp_f32_e32 v4, v109
	v_mul_f32_e32 v118, v51, v67
	v_mul_f32_e32 v119, v35, v67
	v_mul_f32_e32 v120, v19, v67
	v_mul_f32_e32 v69, v14, v3
	v_mul_f32_e32 v70, v62, v3
	v_mul_f32_e32 v68, v46, v3
	v_mul_f32_e32 v67, v30, v3
	v_rcp_f32_e32 v3, v110
	v_mul_f32_e32 v61, v15, v4
	v_mul_f32_e32 v62, v63, v4
	v_mul_f32_e32 v60, v47, v4
	v_mul_f32_e32 v59, v31, v4
	v_rcp_f32_e32 v4, v111
	v_mul_f32_e32 v56, v48, v3
	v_mul_f32_e32 v57, v16, v3
	v_mul_f32_e32 v58, v64, v3
	v_mul_f32_e32 v55, v32, v3
	v_mul_f32_e32 v45, v17, v4
	v_mul_f32_e32 v44, v65, v4
	v_mul_f32_e32 v43, v49, v4
	s_waitcnt vmcnt(3)
	v_mul_f32_e32 v41, 0x3f4ccccd, v50
	v_lshrrev_b32_e32 v50, 1, v0
	v_and_b32_e32 v35, 0xe0, v50
	v_add_u32_e32 v36, s42, v35
	v_mbcnt_lo_u32_b32 v35, -1, 0
	v_mbcnt_hi_u32_b32 v35, -1, v35
	v_and_b32_e32 v47, 64, v35
	v_xor_b32_e32 v46, 1, v35
	v_add_u32_e32 v48, 64, v47
	v_cmp_lt_i32_e32 vcc, v46, v48
	v_mul_f32_e32 v42, v33, v4
	s_waitcnt vmcnt(0)
	v_mul_f32_e32 v38, 0x3f4ccccd, v2
	v_cndmask_b32_e32 v46, v35, v46, vcc
	ds_read_b128 v[26:29], v200
	ds_read_b128 v[10:13], v200 offset:8192
	ds_read_b128 v[30:33], v200 offset:16384
	ds_read_b128 v[14:17], v200 offset:24576
	ds_read_b128 v[22:25], v200 offset:32768
	ds_read_b128 v[6:9], v200 offset:40960
	ds_read_b128 v[18:21], v200 offset:49152
	ds_read_b128 v[2:5], v200 offset:57344
	v_lshlrev_b32_e32 v47, 2, v46
	s_waitcnt lgkmcnt(7)
	v_lshlrev_b32_e32 v46, 16, v26
	v_fma_f32 v64, -v66, v103, v46
	s_waitcnt lgkmcnt(5)
	v_lshlrev_b32_e32 v46, 16, v30
	v_fma_f32 v103, -v66, v112, v46
	v_mul_f32_e32 v46, v103, v103
	s_waitcnt lgkmcnt(3)
	v_lshlrev_b32_e32 v49, 16, v22
	v_fmac_f32_e32 v46, v64, v64
	v_fma_f32 v104, -v66, v115, v49
	s_waitcnt lgkmcnt(1)
	v_lshlrev_b32_e32 v49, 16, v18
	v_fmac_f32_e32 v46, v104, v104
	v_fma_f32 v105, -v66, v116, v49
	v_fmac_f32_e32 v46, v105, v105
	s_nop 1
	v_mov_b32_dpp v51, v46 quad_perm:[1,0,3,2] row_mask:0xf bank_mask:0xf
	v_xor_b32_e32 v49, 2, v35
	v_cmp_lt_i32_e32 vcc, v49, v48
	v_ashrrev_i32_e32 v37, 31, v36
	v_lshlrev_b64 v[36:37], 10, v[36:37]
	v_cndmask_b32_e32 v49, v35, v49, vcc
	v_lshlrev_b32_e32 v49, 2, v49
	s_waitcnt lgkmcnt(0)
	v_add_f32_e32 v46, v46, v51
	s_nop 1
	v_mov_b32_dpp v52, v46 quad_perm:[2,3,0,1] row_mask:0xf bank_mask:0xf
	v_xor_b32_e32 v51, 4, v35
	v_cmp_lt_i32_e32 vcc, v51, v48
	v_lshl_add_u64 v[36:37], s[82:83], 0, v[36:37]
	v_lshl_add_u64 v[178:179], v[36:37], 0, s[38:39]
	v_cndmask_b32_e32 v51, v35, v51, vcc
	v_lshlrev_b32_e32 v51, 2, v51
	s_waitcnt lgkmcnt(0)
	v_add_f32_e32 v46, v46, v52
	s_nop 1
	v_mov_b32_dpp v53, v46 row_shl:4 row_mask:0xf bank_mask:0x5
	s_nop 1
	v_mov_b32_dpp v53, v46 row_shr:4 row_mask:0xf bank_mask:0xa
	v_xor_b32_e32 v52, 8, v35
	v_cmp_lt_i32_e32 vcc, v52, v48
	s_mov_b32 s6, 0xf800000
	v_bfe_u32 v186, v0, 5, 1
	v_cndmask_b32_e32 v52, v35, v52, vcc
	v_lshlrev_b32_e32 v52, 2, v52
	s_waitcnt lgkmcnt(0)
	v_add_f32_e32 v46, v46, v53
	s_nop 1
	v_mov_b32_dpp v54, v46 row_ror:8 row_mask:0xf bank_mask:0xf
	v_xor_b32_e32 v53, 16, v35
	v_cmp_lt_i32_e32 vcc, v53, v48
	v_mov_b32_e32 v34, v172
	v_mov_b32_e32 v63, v186
	v_cndmask_b32_e32 v35, v35, v53, vcc
	v_lshlrev_b32_e32 v53, 2, v35
	s_waitcnt lgkmcnt(0)
	v_add_f32_e32 v46, v46, v54
	v_mov_b32_e32 v48, v46
	s_nop 1
	v_permlane16_swap_b32_e32 v48, v46
	v_and_b32_e32 v30, 0xffff0000, v30
	v_and_b32_e32 v26, 0xffff0000, v26
	v_fma_f32 v30, -v66, v118, v30
	s_waitcnt lgkmcnt(0)
; __device__ __forceinline__ unsigned char f2fp8(float a) { return (unsigned char)(__builtin_amdgcn_cvt_pk_fp8_f32(a, a, 0, false) & 0xff); }
; __device__ __forceinline__ float bf_lo(unsigned w) { return __uint_as_float(w << 16); }
; __device__ __forceinline__ float bf_hi(unsigned w) { return __uint_as_float(w & 0xffff0000u); }
; __device__ __forceinline__ int crow(int r, int hi) { return (r & 3) + 8 * (r >> 2) + 4 * hi; }
; __device__ __forceinline__ void p3_attention(Frame& F) {
;     ...
;         for (int r = 0; r < 16; ++r) {
;             float dd[4], ss = 0.f;
; #pragma unroll
;             for (int d = 0; d < 4; ++d) { const unsigned pw = o1p[d * 2 + (r >> 3)][(r & 7) >> 1]; const float o1 = (r & 1) ? bf_hi(pw) : bf_lo(pw); dd[d] = o1 - lam * o[d][r]; ss += dd[d] * dd[d]; }
;             ss += __shfl_xor(ss, 1); ss += __shfl_xor(ss, 2); ss += __shfl_xor(ss, 4); ss += __shfl_xor(ss, 8); ss += __shfl_xor(ss, 16);
;             const float rs = 1.0f / sqrtf(ss * (1.0f / 128.0f) + RMS_EPS);
;             unsigned char* orow = od + (size_t)attn::crow(r, hi1) * 1024;
; #pragma unroll
;             for (int d = 0; d < 4; ++d) orow[d * 32] = f2fp8(dd[d] * rs * sw[d] * OSCALE);
	v_add_f32_e32 v36, v46, v48
	v_mov_b32_e32 v48, 0x3727c5ac
	v_fmamk_f32 v36, v36, 0x3c000000, v48
	v_mul_f32_e32 v37, 0x4f800000, v36
	v_cmp_gt_f32_e32 vcc, s6, v36
	v_fma_f32 v26, -v66, v117, v26
	v_and_b32_e32 v22, 0xffff0000, v22
	v_cndmask_b32_e32 v36, v36, v37, vcc
	v_sqrt_f32_e32 v37, v36
	v_fma_f32 v22, -v66, v119, v22
	v_and_b32_e32 v18, 0xffff0000, v18
	v_fma_f32 v18, -v66, v120, v18
	v_add_u32_e32 v46, -1, v37
	v_fma_f32 v54, -v46, v37, v36
	v_cmp_ge_f32_e64 s[4:5], 0, v54
	v_add_u32_e32 v54, 1, v37
	v_ashrrev_i32_e32 v35, 31, v34
	v_cndmask_b32_e64 v46, v37, v46, s[4:5]
	v_fma_f32 v37, -v54, v37, v36
	v_cmp_lt_f32_e64 s[4:5], 0, v37
	v_lshl_add_u64 v[34:35], v[178:179], 0, v[34:35]
	s_mov_b64 s[42:43], 0x41600000
	v_cndmask_b32_e64 v37, v46, v54, s[4:5]
	v_mul_f32_e32 v46, 0x37800000, v37
	v_mov_b32_e32 v54, 0x260
	v_cndmask_b32_e32 v37, v37, v46, vcc
	v_cmp_class_f32_e32 vcc, v36, v54
	v_lshl_add_u64 v[34:35], v[34:35], 0, s[42:43]
	v_mul_f32_e32 v40, 0x3f4ccccd, v113
	v_cndmask_b32_e32 v37, v37, v36, vcc
	v_div_scale_f32 v65, s[4:5], v37, v37, 1.0
	v_rcp_f32_e32 v106, v65
	v_lshlrev_b32_e32 v36, 2, v63
	v_mul_f32_e32 v39, 0x3f4ccccd, v114
	v_mov_b32_e32 v46, 0
	v_fma_f32 v63, -v65, v106, 1.0
	v_fmac_f32_e32 v106, v63, v106
	v_div_scale_f32 v63, vcc, 1.0, v37, 1.0
	v_mul_f32_e32 v107, v63, v106
	v_fma_f32 v108, -v65, v107, v63
	v_fmac_f32_e32 v107, v108, v106
	v_fma_f32 v63, -v65, v107, v63
	v_div_fmas_f32 v63, v63, v106, v107
	v_div_fixup_f32 v63, v63, v37, 1.0
	v_mul_f32_e32 v37, v64, v63
	v_mul_f32_e32 v64, v30, v30
	v_fmac_f32_e32 v64, v26, v26
	v_fmac_f32_e32 v64, v22, v22
	v_fmac_f32_e32 v64, v18, v18
	s_nop 1
	v_mov_b32_dpp v65, v64 quad_perm:[1,0,3,2] row_mask:0xf bank_mask:0xf
	v_mul_f32_e32 v37, v41, v37
	v_mul_f32_e32 v37, 0x41800000, v37
	v_mov_b32_e32 v106, 0
	v_cvt_pk_fp8_f32 v106, v37, v37
	s_waitcnt lgkmcnt(0)
	v_add_f32_e32 v107, v64, v65
	s_nop 1
	v_mov_b32_dpp v108, v107 quad_perm:[2,3,0,1] row_mask:0xf bank_mask:0xf
	v_ashrrev_i32_e32 v37, 31, v36
	v_lshlrev_b64 v[64:65], 10, v[36:37]
	v_lshl_add_u64 v[64:65], v[34:35], 0, v[64:65]
	global_store_byte v[64:65], v106, off
	s_waitcnt lgkmcnt(0)
	v_add_f32_e32 v37, v107, v108
	s_nop 1
	v_mov_b32_dpp v106, v37 row_shl:4 row_mask:0xf bank_mask:0x5
	s_nop 1
	v_mov_b32_dpp v106, v37 row_shr:4 row_mask:0xf bank_mask:0xa
	v_mul_f32_e32 v103, v103, v63
	v_mul_f32_e32 v103, v40, v103
	v_mul_f32_e32 v103, 0x41800000, v103
	v_mov_b32_e32 v107, 0
	s_waitcnt lgkmcnt(0)
	v_add_f32_e32 v37, v37, v106
	s_nop 1
	v_mov_b32_dpp v106, v37 row_ror:8 row_mask:0xf bank_mask:0xf
	v_cvt_pk_fp8_f32 v107, v103, v103
	v_mul_f32_e32 v103, v104, v63
	v_mul_f32_e32 v103, v39, v103
	v_mul_f32_e32 v103, 0x41800000, v103
	s_waitcnt lgkmcnt(0)
	v_add_f32_e32 v37, v37, v106
	v_mov_b32_e32 v104, v37
	s_nop 1
	v_permlane16_swap_b32_e32 v104, v37
	v_mov_b32_e32 v106, 0
	v_cvt_pk_fp8_f32 v106, v103, v103
	v_mul_f32_e32 v63, v105, v63
	v_mul_f32_e32 v63, v38, v63
	s_waitcnt lgkmcnt(0)
	v_add_f32_e32 v37, v37, v104
	v_fmamk_f32 v37, v37, 0x3c000000, v48
	v_mul_f32_e32 v103, 0x4f800000, v37
	v_cmp_gt_f32_e32 vcc, s6, v37
	v_mul_f32_e32 v63, 0x41800000, v63
	v_mov_b32_e32 v104, 0
	v_cndmask_b32_e32 v37, v37, v103, vcc
	v_sqrt_f32_e32 v103, v37
	v_cvt_pk_fp8_f32 v104, v63, v63
	global_store_byte v[64:65], v107, off offset:32
	global_store_byte v[64:65], v106, off offset:64
	global_store_byte v[64:65], v104, off offset:96
	v_add_u32_e32 v63, -1, v103
	v_fma_f32 v105, -v63, v103, v37
	v_cmp_ge_f32_e64 s[4:5], 0, v105
	v_add_u32_e32 v105, 1, v103
	v_mov_b32_e32 v107, 0
	v_cndmask_b32_e64 v63, v103, v63, s[4:5]
	v_fma_f32 v103, -v105, v103, v37
	v_cmp_lt_f32_e64 s[4:5], 0, v103
	s_cmp_gt_i32 s55, 14
	s_nop 0
	v_cndmask_b32_e64 v63, v63, v105, s[4:5]
	v_mul_f32_e32 v103, 0x37800000, v63
	v_cndmask_b32_e32 v63, v63, v103, vcc
	v_cmp_class_f32_e32 vcc, v37, v54
	v_lshlrev_b32_e32 v105, 16, v19
	v_fma_f32 v105, -v66, v124, v105
	v_cndmask_b32_e32 v37, v63, v37, vcc
	v_div_scale_f32 v63, s[4:5], v37, v37, 1.0
	v_rcp_f32_e32 v103, v63
	v_and_b32_e32 v19, 0xffff0000, v19
	v_fma_f32 v64, -v63, v103, 1.0
	v_fmac_f32_e32 v103, v64, v103
	v_div_scale_f32 v64, vcc, 1.0, v37, 1.0
	v_mul_f32_e32 v65, v64, v103
	v_fma_f32 v104, -v63, v65, v64
	v_fmac_f32_e32 v65, v104, v103
	v_fma_f32 v63, -v63, v65, v64
	v_div_fmas_f32 v63, v63, v103, v65
	v_lshlrev_b32_e32 v65, 16, v31
	v_div_fixup_f32 v37, v63, v37, 1.0
	v_lshlrev_b32_e32 v63, 16, v27
	v_fma_f32 v103, -v66, v122, v65
	v_fma_f32 v63, -v66, v121, v63
	v_mul_f32_e32 v65, v103, v103
	v_lshlrev_b32_e32 v104, 16, v23
	v_fmac_f32_e32 v65, v63, v63
	v_fma_f32 v104, -v66, v123, v104
	v_fmac_f32_e32 v65, v104, v104
	v_fmac_f32_e32 v65, v105, v105
	s_nop 1
	v_mov_b32_dpp v106, v65 quad_perm:[1,0,3,2] row_mask:0xf bank_mask:0xf
	v_mul_f32_e32 v26, v26, v37
	v_mul_f32_e32 v26, v41, v26
	v_mul_f32_e32 v26, 0x41800000, v26
	v_cvt_pk_fp8_f32 v107, v26, v26
	s_waitcnt lgkmcnt(0)
	v_add_f32_e32 v26, v65, v106
	s_nop 1
	v_mov_b32_dpp v106, v26 quad_perm:[2,3,0,1] row_mask:0xf bank_mask:0xf
	v_or_b32_e32 v64, 1, v36
	v_ashrrev_i32_e32 v65, 31, v64
	v_lshlrev_b64 v[64:65], 10, v[64:65]
	v_mul_f32_e32 v30, v30, v37
	s_waitcnt lgkmcnt(0)
	v_add_f32_e32 v26, v26, v106
	s_nop 1
	v_mov_b32_dpp v106, v26 row_shl:4 row_mask:0xf bank_mask:0x5
	s_nop 1
	v_mov_b32_dpp v106, v26 row_shr:4 row_mask:0xf bank_mask:0xa
	v_lshl_add_u64 v[64:65], v[34:35], 0, v[64:65]
	v_mul_f32_e32 v30, v40, v30
	global_store_byte v[64:65], v107, off
	v_mul_f32_e32 v30, 0x41800000, v30
	s_waitcnt lgkmcnt(0)
; __device__ __forceinline__ unsigned char f2fp8(float a) { return (unsigned char)(__builtin_amdgcn_cvt_pk_fp8_f32(a, a, 0, false) & 0xff); }
; __device__ __forceinline__ float bf_lo(unsigned w) { return __uint_as_float(w << 16); }
; __device__ __forceinline__ float bf_hi(unsigned w) { return __uint_as_float(w & 0xffff0000u); }
; __device__ __forceinline__ int crow(int r, int hi) { return (r & 3) + 8 * (r >> 2) + 4 * hi; }
; __device__ __forceinline__ void p3_attention(Frame& F) {
;     ...
;         for (int r = 0; r < 16; ++r) {
;             float dd[4], ss = 0.f;
; #pragma unroll
;             for (int d = 0; d < 4; ++d) { const unsigned pw = o1p[d * 2 + (r >> 3)][(r & 7) >> 1]; const float o1 = (r & 1) ? bf_hi(pw) : bf_lo(pw); dd[d] = o1 - lam * o[d][r]; ss += dd[d] * dd[d]; }
;             ss += __shfl_xor(ss, 1); ss += __shfl_xor(ss, 2); ss += __shfl_xor(ss, 4); ss += __shfl_xor(ss, 8); ss += __shfl_xor(ss, 16);
;             const float rs = 1.0f / sqrtf(ss * (1.0f / 128.0f) + RMS_EPS);
;             unsigned char* orow = od + (size_t)attn::crow(r, hi1) * 1024;
; #pragma unroll
;             for (int d = 0; d < 4; ++d) orow[d * 32] = f2fp8(dd[d] * rs * sw[d] * OSCALE);
	v_add_f32_e32 v26, v26, v106
	s_nop 1
	v_mov_b32_dpp v106, v26 row_ror:8 row_mask:0xf bank_mask:0xf
	v_mov_b32_e32 v107, 0
	v_cvt_pk_fp8_f32 v107, v30, v30
	v_mul_f32_e32 v22, v22, v37
	v_mul_f32_e32 v22, v39, v22
	s_waitcnt lgkmcnt(0)
	v_add_f32_e32 v26, v26, v106
	v_mov_b32_e32 v30, v26
	s_nop 1
	v_permlane16_swap_b32_e32 v30, v26
	v_mul_f32_e32 v22, 0x41800000, v22
	v_mov_b32_e32 v106, 0
	v_cvt_pk_fp8_f32 v106, v22, v22
	v_mul_f32_e32 v18, v18, v37
	s_waitcnt lgkmcnt(0)
	v_add_f32_e32 v22, v26, v30
	v_fmamk_f32 v22, v22, 0x3c000000, v48
	v_mul_f32_e32 v26, 0x4f800000, v22
	v_cmp_gt_f32_e32 vcc, s6, v22
	v_mul_f32_e32 v18, v38, v18
	v_mul_f32_e32 v18, 0x41800000, v18
	v_cndmask_b32_e32 v22, v22, v26, vcc
	v_sqrt_f32_e32 v26, v22
	v_mov_b32_e32 v30, 0
	v_cvt_pk_fp8_f32 v30, v18, v18
	global_store_byte v[64:65], v107, off offset:32
	global_store_byte v[64:65], v106, off offset:64
	global_store_byte v[64:65], v30, off offset:96
	v_add_u32_e32 v18, -1, v26
	v_fma_f32 v37, -v18, v26, v22
	v_cmp_ge_f32_e64 s[4:5], 0, v37
	v_add_u32_e32 v37, 1, v26
	v_and_b32_e32 v27, 0xffff0000, v27
	v_cndmask_b32_e64 v18, v26, v18, s[4:5]
	v_fma_f32 v26, -v37, v26, v22
	v_cmp_lt_f32_e64 s[4:5], 0, v26
	v_fma_f32 v27, -v66, v125, v27
	v_and_b32_e32 v23, 0xffff0000, v23
	v_cndmask_b32_e64 v18, v18, v37, s[4:5]
	v_mul_f32_e32 v26, 0x37800000, v18
	v_cndmask_b32_e32 v18, v18, v26, vcc
	v_cmp_class_f32_e32 vcc, v22, v54
	v_fma_f32 v23, -v66, v127, v23
	v_mov_b32_e32 v65, 0
	v_cndmask_b32_e32 v18, v18, v22, vcc
	v_div_scale_f32 v22, s[4:5], v18, v18, 1.0
	v_rcp_f32_e32 v26, v22
	s_nop 0
	v_fma_f32 v30, -v22, v26, 1.0
	v_fmac_f32_e32 v26, v30, v26
	v_div_scale_f32 v30, vcc, 1.0, v18, 1.0
	v_mul_f32_e32 v37, v30, v26
	v_fma_f32 v64, -v22, v37, v30
	v_fmac_f32_e32 v37, v64, v26
	v_fma_f32 v22, -v22, v37, v30
	v_and_b32_e32 v30, 0xffff0000, v31
	v_fma_f32 v30, -v66, v126, v30
	v_mul_f32_e32 v31, v30, v30
	v_fmac_f32_e32 v31, v27, v27
	v_div_fmas_f32 v22, v22, v26, v37
	v_fmac_f32_e32 v31, v23, v23
	v_fma_f32 v37, -v66, v128, v19
	v_fmac_f32_e32 v31, v37, v37
	s_nop 1
	v_mov_b32_dpp v19, v31 quad_perm:[1,0,3,2] row_mask:0xf bank_mask:0xf
	v_div_fixup_f32 v22, v22, v18, 1.0
	v_mul_f32_e32 v26, v63, v22
	v_mul_f32_e32 v26, v41, v26
	v_mul_f32_e32 v26, 0x41800000, v26
	v_mov_b32_e32 v63, 0
	v_cvt_pk_fp8_f32 v63, v26, v26
	s_waitcnt lgkmcnt(0)
	v_add_f32_e32 v26, v31, v19
	s_nop 1
	v_mov_b32_dpp v31, v26 quad_perm:[2,3,0,1] row_mask:0xf bank_mask:0xf
	v_or_b32_e32 v18, 2, v36
	v_ashrrev_i32_e32 v19, 31, v18
	v_lshlrev_b64 v[18:19], 10, v[18:19]
	v_lshl_add_u64 v[18:19], v[34:35], 0, v[18:19]
	s_waitcnt lgkmcnt(0)
	v_add_f32_e32 v26, v26, v31
	s_nop 1
	v_mov_b32_dpp v31, v26 row_shl:4 row_mask:0xf bank_mask:0x5
	s_nop 1
	v_mov_b32_dpp v31, v26 row_shr:4 row_mask:0xf bank_mask:0xa
	global_store_byte v[18:19], v63, off
	v_mul_f32_e32 v63, v103, v22
	v_mul_f32_e32 v63, v40, v63
	v_mul_f32_e32 v63, 0x41800000, v63
	s_waitcnt lgkmcnt(0)
	v_add_f32_e32 v26, v26, v31
	s_nop 1
	v_mov_b32_dpp v31, v26 row_ror:8 row_mask:0xf bank_mask:0xf
	v_mov_b32_e32 v64, 0
	v_cvt_pk_fp8_f32 v64, v63, v63
	v_mul_f32_e32 v63, v104, v22
	v_mul_f32_e32 v63, v39, v63
	s_waitcnt lgkmcnt(0)
	v_add_f32_e32 v26, v26, v31
	v_mov_b32_e32 v31, v26
	s_nop 1
	v_permlane16_swap_b32_e32 v31, v26
	v_mul_f32_e32 v22, v105, v22
	v_mul_f32_e32 v63, 0x41800000, v63
	v_mul_f32_e32 v22, v38, v22
	v_cvt_pk_fp8_f32 v65, v63, v63
	s_waitcnt lgkmcnt(0)
	v_add_f32_e32 v26, v26, v31
	v_fmamk_f32 v26, v26, 0x3c000000, v48
	v_mul_f32_e32 v31, 0x4f800000, v26
	v_cmp_gt_f32_e32 vcc, s6, v26
	v_mul_f32_e32 v22, 0x41800000, v22
	v_mov_b32_e32 v63, 0
	v_cndmask_b32_e32 v26, v26, v31, vcc
	v_sqrt_f32_e32 v31, v26
	v_cvt_pk_fp8_f32 v63, v22, v22
	global_store_byte v[18:19], v64, off offset:32
	global_store_byte v[18:19], v65, off offset:64
	global_store_byte v[18:19], v63, off offset:96
	v_add_u32_e32 v22, -1, v31
	v_fma_f32 v103, -v22, v31, v26
	v_cmp_ge_f32_e64 s[4:5], 0, v103
	v_add_u32_e32 v103, 1, v31
	v_lshlrev_b32_e32 v64, 16, v20
	v_cndmask_b32_e64 v22, v31, v22, s[4:5]
	v_fma_f32 v31, -v103, v31, v26
	v_cmp_lt_f32_e64 s[4:5], 0, v31
	v_fma_f32 v64, -v66, v99, v64
	v_mov_b32_e32 v99, 0
	v_cndmask_b32_e64 v22, v22, v103, s[4:5]
	v_mul_f32_e32 v31, 0x37800000, v22
	v_cndmask_b32_e32 v22, v22, v31, vcc
	v_cmp_class_f32_e32 vcc, v26, v54
	v_and_b32_e32 v20, 0xffff0000, v20
	v_fma_f32 v20, -v66, v95, v20
	v_cndmask_b32_e32 v22, v22, v26, vcc
	v_div_scale_f32 v26, s[4:5], v22, v22, 1.0
	v_rcp_f32_e32 v31, v26
	s_nop 0
	v_fma_f32 v18, -v26, v31, 1.0
	v_fmac_f32_e32 v31, v18, v31
	v_div_scale_f32 v18, vcc, 1.0, v22, 1.0
	v_mul_f32_e32 v19, v18, v31
	v_fma_f32 v63, -v26, v19, v18
	v_fmac_f32_e32 v19, v63, v31
	v_fma_f32 v18, -v26, v19, v18
	v_div_fmas_f32 v18, v18, v31, v19
	v_div_fixup_f32 v22, v18, v22, 1.0
	v_mul_f32_e32 v19, v27, v22
	v_lshlrev_b32_e32 v27, 16, v32
	v_lshlrev_b32_e32 v26, 16, v28
	v_fma_f32 v27, -v66, v102, v27
	v_fma_f32 v26, -v66, v101, v26
	v_mul_f32_e32 v31, v27, v27
	v_lshlrev_b32_e32 v63, 16, v24
	v_fmac_f32_e32 v31, v26, v26
	v_fma_f32 v63, -v66, v100, v63
	v_fmac_f32_e32 v31, v63, v63
	v_fmac_f32_e32 v31, v64, v64
	s_nop 1
	v_mov_b32_dpp v65, v31 quad_perm:[1,0,3,2] row_mask:0xf bank_mask:0xf
	v_mul_f32_e32 v19, v41, v19
	v_mul_f32_e32 v19, 0x41800000, v19
	v_or_b32_e32 v18, 3, v36
	v_cvt_pk_fp8_f32 v99, v19, v19
	s_waitcnt lgkmcnt(0)
	v_add_f32_e32 v31, v31, v65
	s_nop 1
	v_mov_b32_dpp v65, v31 quad_perm:[2,3,0,1] row_mask:0xf bank_mask:0xf
	v_ashrrev_i32_e32 v19, 31, v18
	v_lshlrev_b64 v[18:19], 10, v[18:19]
	v_mul_f32_e32 v30, v30, v22
	v_lshl_add_u64 v[18:19], v[34:35], 0, v[18:19]
	s_waitcnt lgkmcnt(0)
; __device__ __forceinline__ unsigned char f2fp8(float a) { return (unsigned char)(__builtin_amdgcn_cvt_pk_fp8_f32(a, a, 0, false) & 0xff); }
; __device__ __forceinline__ float bf_lo(unsigned w) { return __uint_as_float(w << 16); }
; __device__ __forceinline__ float bf_hi(unsigned w) { return __uint_as_float(w & 0xffff0000u); }
; __device__ __forceinline__ int crow(int r, int hi) { return (r & 3) + 8 * (r >> 2) + 4 * hi; }
; __device__ __forceinline__ void p3_attention(Frame& F) {
;     ...
;         for (int r = 0; r < 16; ++r) {
;             float dd[4], ss = 0.f;
; #pragma unroll
;             for (int d = 0; d < 4; ++d) { const unsigned pw = o1p[d * 2 + (r >> 3)][(r & 7) >> 1]; const float o1 = (r & 1) ? bf_hi(pw) : bf_lo(pw); dd[d] = o1 - lam * o[d][r]; ss += dd[d] * dd[d]; }
;             ss += __shfl_xor(ss, 1); ss += __shfl_xor(ss, 2); ss += __shfl_xor(ss, 4); ss += __shfl_xor(ss, 8); ss += __shfl_xor(ss, 16);
;             const float rs = 1.0f / sqrtf(ss * (1.0f / 128.0f) + RMS_EPS);
;             unsigned char* orow = od + (size_t)attn::crow(r, hi1) * 1024;
; #pragma unroll
;             for (int d = 0; d < 4; ++d) orow[d * 32] = f2fp8(dd[d] * rs * sw[d] * OSCALE);
	v_add_f32_e32 v31, v31, v65
	s_nop 1
	v_mov_b32_dpp v65, v31 row_shl:4 row_mask:0xf bank_mask:0x5
	s_nop 1
	v_mov_b32_dpp v65, v31 row_shr:4 row_mask:0xf bank_mask:0xa
	v_mul_f32_e32 v30, v40, v30
	global_store_byte v[18:19], v99, off
	v_mul_f32_e32 v30, 0x41800000, v30
	v_mov_b32_e32 v99, 0
	s_waitcnt lgkmcnt(0)
	v_add_f32_e32 v31, v31, v65
	s_nop 1
	v_mov_b32_dpp v65, v31 row_ror:8 row_mask:0xf bank_mask:0xf
	v_cvt_pk_fp8_f32 v99, v30, v30
	v_mul_f32_e32 v23, v23, v22
	v_mul_f32_e32 v23, v39, v23
	v_mul_f32_e32 v23, 0x41800000, v23
	s_waitcnt lgkmcnt(0)
	v_add_f32_e32 v30, v31, v65
	v_mov_b32_e32 v31, v30
	s_nop 1
	v_permlane16_swap_b32_e32 v31, v30
	v_mov_b32_e32 v65, 0
	v_cvt_pk_fp8_f32 v65, v23, v23
	v_mul_f32_e32 v22, v37, v22
	v_mul_f32_e32 v22, v38, v22
	s_waitcnt lgkmcnt(0)
	v_add_f32_e32 v23, v30, v31
	v_fmamk_f32 v23, v23, 0x3c000000, v48
	v_mul_f32_e32 v30, 0x4f800000, v23
	v_cmp_gt_f32_e32 vcc, s6, v23
	v_mul_f32_e32 v22, 0x41800000, v22
	v_mov_b32_e32 v31, 0
	v_cndmask_b32_e32 v23, v23, v30, vcc
	v_sqrt_f32_e32 v30, v23
	v_cvt_pk_fp8_f32 v31, v22, v22
	global_store_byte v[18:19], v99, off offset:32
	global_store_byte v[18:19], v65, off offset:64
	global_store_byte v[18:19], v31, off offset:96
	v_add_u32_e32 v22, -1, v30
	v_fma_f32 v37, -v22, v30, v23
	v_cmp_ge_f32_e64 s[4:5], 0, v37
	v_add_u32_e32 v37, 1, v30
	v_and_b32_e32 v24, 0xffff0000, v24
	v_cndmask_b32_e64 v22, v30, v22, s[4:5]
	v_fma_f32 v30, -v37, v30, v23
	v_cmp_lt_f32_e64 s[4:5], 0, v30
	v_fma_f32 v24, -v66, v96, v24
	s_nop 0
	v_cndmask_b32_e64 v22, v22, v37, s[4:5]
	v_mul_f32_e32 v30, 0x37800000, v22
	v_cndmask_b32_e32 v22, v22, v30, vcc
	v_cmp_class_f32_e32 vcc, v23, v54
	s_nop 1
	v_cndmask_b32_e32 v22, v22, v23, vcc
	v_div_scale_f32 v23, s[4:5], v22, v22, 1.0
	v_rcp_f32_e32 v30, v23
	s_nop 0
	v_fma_f32 v18, -v23, v30, 1.0
	v_fmac_f32_e32 v30, v18, v30
	v_div_scale_f32 v18, vcc, 1.0, v22, 1.0
	v_mul_f32_e32 v19, v18, v30
	v_fma_f32 v31, -v23, v19, v18
	v_fmac_f32_e32 v19, v31, v30
	v_fma_f32 v18, -v23, v19, v18
	v_div_fmas_f32 v18, v18, v30, v19
	v_div_fixup_f32 v22, v18, v22, 1.0
	v_mul_f32_e32 v19, v26, v22
	v_and_b32_e32 v26, 0xffff0000, v32
	v_and_b32_e32 v23, 0xffff0000, v28
	v_fma_f32 v26, -v66, v98, v26
	v_fma_f32 v23, -v66, v97, v23
	v_mul_f32_e32 v28, v26, v26
	v_fmac_f32_e32 v28, v23, v23
	v_fmac_f32_e32 v28, v24, v24
	v_fmac_f32_e32 v28, v20, v20
	s_nop 1
	v_mov_b32_dpp v30, v28 quad_perm:[1,0,3,2] row_mask:0xf bank_mask:0xf
	v_mul_f32_e32 v19, v41, v19
	v_mul_f32_e32 v19, 0x41800000, v19
	v_mov_b32_e32 v31, 0
	v_add_u32_e32 v18, 8, v36
	s_waitcnt lgkmcnt(0)
	v_add_f32_e32 v28, v28, v30
	s_nop 1
	v_mov_b32_dpp v30, v28 quad_perm:[2,3,0,1] row_mask:0xf bank_mask:0xf
	v_cvt_pk_fp8_f32 v31, v19, v19
	v_ashrrev_i32_e32 v19, 31, v18
	v_lshlrev_b64 v[18:19], 10, v[18:19]
	v_mul_f32_e32 v27, v27, v22
	s_waitcnt lgkmcnt(0)
	v_add_f32_e32 v28, v28, v30
	s_nop 1
	v_mov_b32_dpp v30, v28 row_shl:4 row_mask:0xf bank_mask:0x5
	s_nop 1
	v_mov_b32_dpp v30, v28 row_shr:4 row_mask:0xf bank_mask:0xa
	v_lshl_add_u64 v[18:19], v[34:35], 0, v[18:19]
	v_mul_f32_e32 v27, v40, v27
	global_store_byte v[18:19], v31, off
	v_mul_f32_e32 v27, 0x41800000, v27
	s_waitcnt lgkmcnt(0)
	v_add_f32_e32 v28, v28, v30
	s_nop 1
	v_mov_b32_dpp v30, v28 row_ror:8 row_mask:0xf bank_mask:0xf
	v_mov_b32_e32 v31, 0
	v_cvt_pk_fp8_f32 v31, v27, v27
	v_mul_f32_e32 v27, v63, v22
	v_mul_f32_e32 v27, v39, v27
	s_waitcnt lgkmcnt(0)
	v_add_f32_e32 v28, v28, v30
	v_mov_b32_e32 v30, v28
	s_nop 1
	v_permlane16_swap_b32_e32 v30, v28
	v_mul_f32_e32 v27, 0x41800000, v27
	v_mov_b32_e32 v32, 0
	v_cvt_pk_fp8_f32 v32, v27, v27
	v_mul_f32_e32 v22, v64, v22
	s_waitcnt lgkmcnt(0)
	v_add_f32_e32 v27, v28, v30
	v_fmamk_f32 v27, v27, 0x3c000000, v48
	v_mul_f32_e32 v28, 0x4f800000, v27
	v_cmp_gt_f32_e32 vcc, s6, v27
	v_mul_f32_e32 v22, v38, v22
	v_mul_f32_e32 v22, 0x41800000, v22
	v_cndmask_b32_e32 v27, v27, v28, vcc
	v_sqrt_f32_e32 v28, v27
	v_mov_b32_e32 v30, 0
	v_cvt_pk_fp8_f32 v30, v22, v22
	global_store_byte v[18:19], v31, off offset:32
	global_store_byte v[18:19], v32, off offset:64
	global_store_byte v[18:19], v30, off offset:96
	v_add_u32_e32 v22, -1, v28
	v_fma_f32 v37, -v22, v28, v27
	v_cmp_ge_f32_e64 s[4:5], 0, v37
	v_add_u32_e32 v37, 1, v28
	v_lshlrev_b32_e32 v31, 16, v21
	v_cndmask_b32_e64 v22, v28, v22, s[4:5]
	v_fma_f32 v28, -v37, v28, v27
	v_cmp_lt_f32_e64 s[4:5], 0, v28
	v_fma_f32 v31, -v66, v91, v31
	v_and_b32_e32 v21, 0xffff0000, v21
	v_cndmask_b32_e64 v22, v22, v37, s[4:5]
	v_mul_f32_e32 v28, 0x37800000, v22
	v_cndmask_b32_e32 v22, v22, v28, vcc
	v_cmp_class_f32_e32 vcc, v27, v54
	v_mov_b32_e32 v37, 0
	v_fma_f32 v21, -v66, v87, v21
	v_cndmask_b32_e32 v22, v22, v27, vcc
	v_div_scale_f32 v27, s[4:5], v22, v22, 1.0
	v_rcp_f32_e32 v28, v27
	s_nop 0
	v_fma_f32 v18, -v27, v28, 1.0
	v_fmac_f32_e32 v28, v18, v28
	v_div_scale_f32 v18, vcc, 1.0, v22, 1.0
	v_mul_f32_e32 v19, v18, v28
	v_fma_f32 v30, -v27, v19, v18
	v_fmac_f32_e32 v19, v30, v28
	v_fma_f32 v18, -v27, v19, v18
	v_div_fmas_f32 v18, v18, v28, v19
	v_div_fixup_f32 v22, v18, v22, 1.0
	v_lshlrev_b32_e32 v27, 16, v33
	v_mul_f32_e32 v19, v23, v22
	v_lshlrev_b32_e32 v23, 16, v29
	v_fma_f32 v27, -v66, v94, v27
	v_fma_f32 v23, -v66, v93, v23
	v_mul_f32_e32 v28, v27, v27
	v_lshlrev_b32_e32 v30, 16, v25
	v_fmac_f32_e32 v28, v23, v23
	v_fma_f32 v30, -v66, v92, v30
	v_fmac_f32_e32 v28, v30, v30
	v_fmac_f32_e32 v28, v31, v31
	s_nop 1
	v_mov_b32_dpp v32, v28 quad_perm:[1,0,3,2] row_mask:0xf bank_mask:0xf
	v_mul_f32_e32 v19, v41, v19
	v_mul_f32_e32 v19, 0x41800000, v19
	v_add_u32_e32 v18, 9, v36
	v_cvt_pk_fp8_f32 v37, v19, v19
	s_waitcnt lgkmcnt(0)
; __device__ __forceinline__ unsigned char f2fp8(float a) { return (unsigned char)(__builtin_amdgcn_cvt_pk_fp8_f32(a, a, 0, false) & 0xff); }
; __device__ __forceinline__ float bf_lo(unsigned w) { return __uint_as_float(w << 16); }
; __device__ __forceinline__ float bf_hi(unsigned w) { return __uint_as_float(w & 0xffff0000u); }
; __device__ __forceinline__ int crow(int r, int hi) { return (r & 3) + 8 * (r >> 2) + 4 * hi; }
; __device__ __forceinline__ void p3_attention(Frame& F) {
;     ...
;         for (int r = 0; r < 16; ++r) {
;             float dd[4], ss = 0.f;
; #pragma unroll
;             for (int d = 0; d < 4; ++d) { const unsigned pw = o1p[d * 2 + (r >> 3)][(r & 7) >> 1]; const float o1 = (r & 1) ? bf_hi(pw) : bf_lo(pw); dd[d] = o1 - lam * o[d][r]; ss += dd[d] * dd[d]; }
;             ss += __shfl_xor(ss, 1); ss += __shfl_xor(ss, 2); ss += __shfl_xor(ss, 4); ss += __shfl_xor(ss, 8); ss += __shfl_xor(ss, 16);
;             const float rs = 1.0f / sqrtf(ss * (1.0f / 128.0f) + RMS_EPS);
;             unsigned char* orow = od + (size_t)attn::crow(r, hi1) * 1024;
; #pragma unroll
;             for (int d = 0; d < 4; ++d) orow[d * 32] = f2fp8(dd[d] * rs * sw[d] * OSCALE);
	v_add_f32_e32 v28, v28, v32
	s_nop 1
	v_mov_b32_dpp v32, v28 quad_perm:[2,3,0,1] row_mask:0xf bank_mask:0xf
	v_ashrrev_i32_e32 v19, 31, v18
	v_lshlrev_b64 v[18:19], 10, v[18:19]
	v_mul_f32_e32 v26, v26, v22
	v_lshl_add_u64 v[18:19], v[34:35], 0, v[18:19]
	s_waitcnt lgkmcnt(0)
	v_add_f32_e32 v28, v28, v32
	s_nop 1
	v_mov_b32_dpp v32, v28 row_shl:4 row_mask:0xf bank_mask:0x5
	s_nop 1
	v_mov_b32_dpp v32, v28 row_shr:4 row_mask:0xf bank_mask:0xa
	v_mul_f32_e32 v26, v40, v26
	global_store_byte v[18:19], v37, off
	v_mul_f32_e32 v26, 0x41800000, v26
	v_mov_b32_e32 v37, 0
	s_waitcnt lgkmcnt(0)
	v_add_f32_e32 v28, v28, v32
	s_nop 1
	v_mov_b32_dpp v32, v28 row_ror:8 row_mask:0xf bank_mask:0xf
	v_cvt_pk_fp8_f32 v37, v26, v26
	v_mul_f32_e32 v24, v24, v22
	v_mul_f32_e32 v24, v39, v24
	v_mul_f32_e32 v20, v20, v22
	s_waitcnt lgkmcnt(0)
	v_add_f32_e32 v26, v28, v32
	v_mov_b32_e32 v28, v26
	s_nop 1
	v_permlane16_swap_b32_e32 v28, v26
	v_mul_f32_e32 v24, 0x41800000, v24
	v_mov_b32_e32 v32, 0
	v_cvt_pk_fp8_f32 v32, v24, v24
	v_mul_f32_e32 v20, v38, v20
	s_waitcnt lgkmcnt(0)
	v_add_f32_e32 v22, v26, v28
	v_fmamk_f32 v22, v22, 0x3c000000, v48
	v_mul_f32_e32 v24, 0x4f800000, v22
	v_cmp_gt_f32_e32 vcc, s6, v22
	v_mul_f32_e32 v20, 0x41800000, v20
	v_mov_b32_e32 v26, 0
	v_cndmask_b32_e32 v22, v22, v24, vcc
	v_sqrt_f32_e32 v24, v22
	v_cvt_pk_fp8_f32 v26, v20, v20
	global_store_byte v[18:19], v37, off offset:32
	global_store_byte v[18:19], v32, off offset:64
	global_store_byte v[18:19], v26, off offset:96
	v_add_u32_e32 v20, -1, v24
	v_fma_f32 v28, -v20, v24, v22
	v_cmp_ge_f32_e64 s[4:5], 0, v28
	v_add_u32_e32 v28, 1, v24
	v_and_b32_e32 v25, 0xffff0000, v25
	v_cndmask_b32_e64 v20, v24, v20, s[4:5]
	v_fma_f32 v24, -v28, v24, v22
	v_cmp_lt_f32_e64 s[4:5], 0, v24
	v_fma_f32 v25, -v66, v88, v25
	s_nop 0
	v_cndmask_b32_e64 v20, v20, v28, s[4:5]
	v_mul_f32_e32 v24, 0x37800000, v20
	v_cndmask_b32_e32 v20, v20, v24, vcc
	v_cmp_class_f32_e32 vcc, v22, v54
	v_mov_b32_e32 v28, 0
	s_nop 0
	v_cndmask_b32_e32 v20, v20, v22, vcc
	v_div_scale_f32 v22, s[4:5], v20, v20, 1.0
	v_rcp_f32_e32 v24, v22
	s_nop 0
	v_fma_f32 v18, -v22, v24, 1.0
	v_fmac_f32_e32 v24, v18, v24
	v_div_scale_f32 v18, vcc, 1.0, v20, 1.0
	v_mul_f32_e32 v19, v18, v24
	v_fma_f32 v26, -v22, v19, v18
	v_fmac_f32_e32 v19, v26, v24
	v_fma_f32 v18, -v22, v19, v18
	v_div_fmas_f32 v18, v18, v24, v19
	v_div_fixup_f32 v20, v18, v20, 1.0
	v_mul_f32_e32 v19, v23, v20
	v_and_b32_e32 v23, 0xffff0000, v33
	v_and_b32_e32 v22, 0xffff0000, v29
	v_fma_f32 v23, -v66, v90, v23
	v_fma_f32 v22, -v66, v89, v22
	v_mul_f32_e32 v24, v23, v23
	v_fmac_f32_e32 v24, v22, v22
	v_fmac_f32_e32 v24, v25, v25
	v_fmac_f32_e32 v24, v21, v21
	s_nop 1
	v_mov_b32_dpp v26, v24 quad_perm:[1,0,3,2] row_mask:0xf bank_mask:0xf
	v_mul_f32_e32 v19, v41, v19
	v_mul_f32_e32 v19, 0x41800000, v19
	v_add_u32_e32 v18, 10, v36
	v_cvt_pk_fp8_f32 v28, v19, v19
	s_waitcnt lgkmcnt(0)
	v_add_f32_e32 v24, v24, v26
	s_nop 1
	v_mov_b32_dpp v26, v24 quad_perm:[2,3,0,1] row_mask:0xf bank_mask:0xf
	v_ashrrev_i32_e32 v19, 31, v18
	v_lshlrev_b64 v[18:19], 10, v[18:19]
	v_mul_f32_e32 v27, v27, v20
	v_lshl_add_u64 v[18:19], v[34:35], 0, v[18:19]
	s_waitcnt lgkmcnt(0)
	v_add_f32_e32 v24, v24, v26
	s_nop 1
	v_mov_b32_dpp v26, v24 row_shl:4 row_mask:0xf bank_mask:0x5
	s_nop 1
	v_mov_b32_dpp v26, v24 row_shr:4 row_mask:0xf bank_mask:0xa
	v_mul_f32_e32 v27, v40, v27
	global_store_byte v[18:19], v28, off
	v_mul_f32_e32 v27, 0x41800000, v27
	v_mov_b32_e32 v28, 0
	s_waitcnt lgkmcnt(0)
	v_add_f32_e32 v24, v24, v26
	s_nop 1
	v_mov_b32_dpp v26, v24 row_ror:8 row_mask:0xf bank_mask:0xf
	v_cvt_pk_fp8_f32 v28, v27, v27
	v_mul_f32_e32 v27, v30, v20
	v_mul_f32_e32 v27, v39, v27
	v_mul_f32_e32 v20, v31, v20
	s_waitcnt lgkmcnt(0)
	v_add_f32_e32 v24, v24, v26
	v_mov_b32_e32 v26, v24
	s_nop 1
	v_permlane16_swap_b32_e32 v26, v24
	v_mul_f32_e32 v27, 0x41800000, v27
	v_mov_b32_e32 v29, 0
	v_mul_f32_e32 v20, v38, v20
	v_cvt_pk_fp8_f32 v29, v27, v27
	s_waitcnt lgkmcnt(0)
	v_add_f32_e32 v24, v24, v26
	v_fmamk_f32 v24, v24, 0x3c000000, v48
	v_mul_f32_e32 v26, 0x4f800000, v24
	v_cmp_gt_f32_e32 vcc, s6, v24
	v_mul_f32_e32 v20, 0x41800000, v20
	v_mov_b32_e32 v27, 0
	v_cndmask_b32_e32 v24, v24, v26, vcc
	v_sqrt_f32_e32 v26, v24
	v_cvt_pk_fp8_f32 v27, v20, v20
	global_store_byte v[18:19], v28, off offset:32
	global_store_byte v[18:19], v29, off offset:64
	global_store_byte v[18:19], v27, off offset:96
	v_add_u32_e32 v20, -1, v26
	v_fma_f32 v30, -v20, v26, v24
	v_cmp_ge_f32_e64 s[4:5], 0, v30
	v_add_u32_e32 v30, 1, v26
	v_lshlrev_b32_e32 v28, 16, v2
	v_cndmask_b32_e64 v20, v26, v20, s[4:5]
	v_fma_f32 v26, -v30, v26, v24
	v_cmp_lt_f32_e64 s[4:5], 0, v26
	v_fma_f32 v28, -v66, v83, v28
	v_and_b32_e32 v2, 0xffff0000, v2
	v_cndmask_b32_e64 v20, v20, v30, s[4:5]
	v_mul_f32_e32 v26, 0x37800000, v20
	v_cndmask_b32_e32 v20, v20, v26, vcc
	v_cmp_class_f32_e32 vcc, v24, v54
	v_mov_b32_e32 v30, 0
	v_fma_f32 v2, -v66, v79, v2
	v_cndmask_b32_e32 v20, v20, v24, vcc
	v_div_scale_f32 v24, s[4:5], v20, v20, 1.0
	v_rcp_f32_e32 v26, v24
	s_nop 0
	v_fma_f32 v18, -v24, v26, 1.0
	v_fmac_f32_e32 v26, v18, v26
	v_div_scale_f32 v18, vcc, 1.0, v20, 1.0
	v_mul_f32_e32 v19, v18, v26
	v_fma_f32 v27, -v24, v19, v18
	v_fmac_f32_e32 v19, v27, v26
	v_fma_f32 v18, -v24, v19, v18
	v_div_fmas_f32 v18, v18, v26, v19
	v_div_fixup_f32 v20, v18, v20, 1.0
	v_lshlrev_b32_e32 v24, 16, v14
	v_mul_f32_e32 v19, v22, v20
	v_lshlrev_b32_e32 v22, 16, v10
	v_fma_f32 v24, -v66, v86, v24
	v_fma_f32 v22, -v66, v85, v22
	v_mul_f32_e32 v26, v24, v24
	v_lshlrev_b32_e32 v27, 16, v6
	v_fmac_f32_e32 v26, v22, v22
	v_fma_f32 v27, -v66, v84, v27
	v_fmac_f32_e32 v26, v27, v27
	v_fmac_f32_e32 v26, v28, v28
	s_nop 1
	v_mov_b32_dpp v29, v26 quad_perm:[1,0,3,2] row_mask:0xf bank_mask:0xf
	v_mul_f32_e32 v19, v41, v19
	v_mul_f32_e32 v19, 0x41800000, v19
	v_add_u32_e32 v18, 11, v36
	v_cvt_pk_fp8_f32 v30, v19, v19
	s_waitcnt lgkmcnt(0)
; __device__ __forceinline__ unsigned char f2fp8(float a) { return (unsigned char)(__builtin_amdgcn_cvt_pk_fp8_f32(a, a, 0, false) & 0xff); }
; __device__ __forceinline__ float bf_lo(unsigned w) { return __uint_as_float(w << 16); }
; __device__ __forceinline__ float bf_hi(unsigned w) { return __uint_as_float(w & 0xffff0000u); }
; __device__ __forceinline__ int crow(int r, int hi) { return (r & 3) + 8 * (r >> 2) + 4 * hi; }
; __device__ __forceinline__ void p3_attention(Frame& F) {
;     ...
;         for (int r = 0; r < 16; ++r) {
;             float dd[4], ss = 0.f;
; #pragma unroll
;             for (int d = 0; d < 4; ++d) { const unsigned pw = o1p[d * 2 + (r >> 3)][(r & 7) >> 1]; const float o1 = (r & 1) ? bf_hi(pw) : bf_lo(pw); dd[d] = o1 - lam * o[d][r]; ss += dd[d] * dd[d]; }
;             ss += __shfl_xor(ss, 1); ss += __shfl_xor(ss, 2); ss += __shfl_xor(ss, 4); ss += __shfl_xor(ss, 8); ss += __shfl_xor(ss, 16);
;             const float rs = 1.0f / sqrtf(ss * (1.0f / 128.0f) + RMS_EPS);
;             unsigned char* orow = od + (size_t)attn::crow(r, hi1) * 1024;
; #pragma unroll
;             for (int d = 0; d < 4; ++d) orow[d * 32] = f2fp8(dd[d] * rs * sw[d] * OSCALE);
	v_add_f32_e32 v26, v26, v29
	s_nop 1
	v_mov_b32_dpp v29, v26 quad_perm:[2,3,0,1] row_mask:0xf bank_mask:0xf
	v_ashrrev_i32_e32 v19, 31, v18
	v_lshlrev_b64 v[18:19], 10, v[18:19]
	v_mul_f32_e32 v23, v23, v20
	v_lshl_add_u64 v[18:19], v[34:35], 0, v[18:19]
	s_waitcnt lgkmcnt(0)
	v_add_f32_e32 v26, v26, v29
	s_nop 1
	v_mov_b32_dpp v29, v26 row_shl:4 row_mask:0xf bank_mask:0x5
	s_nop 1
	v_mov_b32_dpp v29, v26 row_shr:4 row_mask:0xf bank_mask:0xa
	v_mul_f32_e32 v23, v40, v23
	global_store_byte v[18:19], v30, off
	v_mul_f32_e32 v23, 0x41800000, v23
	v_mov_b32_e32 v30, 0
	s_waitcnt lgkmcnt(0)
	v_add_f32_e32 v26, v26, v29
	s_nop 1
	v_mov_b32_dpp v29, v26 row_ror:8 row_mask:0xf bank_mask:0xf
	v_cvt_pk_fp8_f32 v30, v23, v23
	v_mul_f32_e32 v23, v25, v20
	v_mul_f32_e32 v23, v39, v23
	v_mul_f32_e32 v20, v21, v20
	s_waitcnt lgkmcnt(0)
	v_add_f32_e32 v25, v26, v29
	v_mov_b32_e32 v26, v25
	s_nop 1
	v_permlane16_swap_b32_e32 v26, v25
	v_mul_f32_e32 v23, 0x41800000, v23
	v_mov_b32_e32 v29, 0
	v_cvt_pk_fp8_f32 v29, v23, v23
	v_mul_f32_e32 v20, v38, v20
	s_waitcnt lgkmcnt(0)
	v_add_f32_e32 v21, v25, v26
	v_fmamk_f32 v21, v21, 0x3c000000, v48
	v_mul_f32_e32 v23, 0x4f800000, v21
	v_cmp_gt_f32_e32 vcc, s6, v21
	v_mul_f32_e32 v20, 0x41800000, v20
	v_mov_b32_e32 v25, 0
	v_cndmask_b32_e32 v21, v21, v23, vcc
	v_sqrt_f32_e32 v23, v21
	v_cvt_pk_fp8_f32 v25, v20, v20
	global_store_byte v[18:19], v30, off offset:32
	global_store_byte v[18:19], v29, off offset:64
	global_store_byte v[18:19], v25, off offset:96
	v_add_u32_e32 v20, -1, v23
	v_fma_f32 v26, -v20, v23, v21
	v_cmp_ge_f32_e64 s[4:5], 0, v26
	v_add_u32_e32 v26, 1, v23
	v_and_b32_e32 v14, 0xffff0000, v14
	v_cndmask_b32_e64 v20, v23, v20, s[4:5]
	v_fma_f32 v23, -v26, v23, v21
	v_cmp_lt_f32_e64 s[4:5], 0, v23
	v_and_b32_e32 v10, 0xffff0000, v10
	v_fma_f32 v14, -v66, v82, v14
	v_cndmask_b32_e64 v20, v20, v26, s[4:5]
	v_mul_f32_e32 v23, 0x37800000, v20
	v_cndmask_b32_e32 v20, v20, v23, vcc
	v_cmp_class_f32_e32 vcc, v21, v54
	v_fma_f32 v10, -v66, v81, v10
	v_and_b32_e32 v6, 0xffff0000, v6
	v_cndmask_b32_e32 v20, v20, v21, vcc
	v_div_scale_f32 v21, s[4:5], v20, v20, 1.0
	v_rcp_f32_e32 v23, v21
	v_fma_f32 v6, -v66, v80, v6
	v_fma_f32 v18, -v21, v23, 1.0
	v_fmac_f32_e32 v23, v18, v23
	v_div_scale_f32 v18, vcc, 1.0, v20, 1.0
	v_mul_f32_e32 v19, v18, v23
	v_fma_f32 v25, -v21, v19, v18
	v_fmac_f32_e32 v19, v25, v23
	v_fma_f32 v18, -v21, v19, v18
	v_mul_f32_e32 v21, v14, v14
	v_fmac_f32_e32 v21, v10, v10
	v_div_fmas_f32 v18, v18, v23, v19
	v_fmac_f32_e32 v21, v6, v6
	v_div_fixup_f32 v20, v18, v20, 1.0
	v_fmac_f32_e32 v21, v2, v2
	v_mul_f32_e32 v19, v22, v20
	s_nop 1
	v_mov_b32_dpp v22, v21 quad_perm:[1,0,3,2] row_mask:0xf bank_mask:0xf
	v_mul_f32_e32 v19, v41, v19
	v_mul_f32_e32 v19, 0x41800000, v19
	v_mov_b32_e32 v23, 0
	v_add_u32_e32 v18, 16, v36
	s_waitcnt lgkmcnt(0)
	v_add_f32_e32 v21, v21, v22
	s_nop 1
	v_mov_b32_dpp v22, v21 quad_perm:[2,3,0,1] row_mask:0xf bank_mask:0xf
	v_cvt_pk_fp8_f32 v23, v19, v19
	v_ashrrev_i32_e32 v19, 31, v18
	v_lshlrev_b64 v[18:19], 10, v[18:19]
	v_lshl_add_u64 v[18:19], v[34:35], 0, v[18:19]
	s_waitcnt lgkmcnt(0)
	v_add_f32_e32 v21, v21, v22
	s_nop 1
	v_mov_b32_dpp v22, v21 row_shl:4 row_mask:0xf bank_mask:0x5
	s_nop 1
	v_mov_b32_dpp v22, v21 row_shr:4 row_mask:0xf bank_mask:0xa
	global_store_byte v[18:19], v23, off
	v_mul_f32_e32 v23, v24, v20
	v_mul_f32_e32 v23, v40, v23
	v_mul_f32_e32 v23, 0x41800000, v23
	s_waitcnt lgkmcnt(0)
	v_add_f32_e32 v21, v21, v22
	s_nop 1
	v_mov_b32_dpp v22, v21 row_ror:8 row_mask:0xf bank_mask:0xf
	v_mov_b32_e32 v24, 0
	v_cvt_pk_fp8_f32 v24, v23, v23
	v_mul_f32_e32 v23, v27, v20
	v_mul_f32_e32 v23, v39, v23
	s_waitcnt lgkmcnt(0)
	v_add_f32_e32 v21, v21, v22
	v_mov_b32_e32 v22, v21
	s_nop 1
	v_permlane16_swap_b32_e32 v22, v21
	v_mul_f32_e32 v20, v28, v20
	v_mul_f32_e32 v23, 0x41800000, v23
	v_mov_b32_e32 v25, 0
	v_mul_f32_e32 v20, v38, v20
	s_waitcnt lgkmcnt(0)
	v_add_f32_e32 v21, v21, v22
	v_fmamk_f32 v21, v21, 0x3c000000, v48
	v_mul_f32_e32 v22, 0x4f800000, v21
	v_cmp_gt_f32_e32 vcc, s6, v21
	v_cvt_pk_fp8_f32 v25, v23, v23
	v_mul_f32_e32 v20, 0x41800000, v20
	v_cndmask_b32_e32 v21, v21, v22, vcc
	v_sqrt_f32_e32 v22, v21
	v_mov_b32_e32 v23, 0
	v_cvt_pk_fp8_f32 v23, v20, v20
	global_store_byte v[18:19], v24, off offset:32
	global_store_byte v[18:19], v25, off offset:64
	global_store_byte v[18:19], v23, off offset:96
	v_add_u32_e32 v20, -1, v22
	v_fma_f32 v26, -v20, v22, v21
	v_cmp_ge_f32_e64 s[4:5], 0, v26
	v_add_u32_e32 v26, 1, v22
	v_lshlrev_b32_e32 v24, 16, v3
	v_cndmask_b32_e64 v20, v22, v20, s[4:5]
	v_fma_f32 v22, -v26, v22, v21
	v_cmp_lt_f32_e64 s[4:5], 0, v22
	v_fma_f32 v24, -v66, v75, v24
	v_and_b32_e32 v3, 0xffff0000, v3
	v_cndmask_b32_e64 v20, v20, v26, s[4:5]
	v_mul_f32_e32 v22, 0x37800000, v20
	v_cndmask_b32_e32 v20, v20, v22, vcc
	v_cmp_class_f32_e32 vcc, v21, v54
	v_mov_b32_e32 v26, 0
	s_nop 0
	v_cndmask_b32_e32 v20, v20, v21, vcc
	v_div_scale_f32 v21, s[4:5], v20, v20, 1.0
	v_rcp_f32_e32 v22, v21
	s_nop 0
	v_fma_f32 v18, -v21, v22, 1.0
	v_fmac_f32_e32 v22, v18, v22
	v_div_scale_f32 v18, vcc, 1.0, v20, 1.0
	v_mul_f32_e32 v19, v18, v22
	v_fma_f32 v23, -v21, v19, v18
	v_fmac_f32_e32 v19, v23, v22
	v_fma_f32 v18, -v21, v19, v18
	v_div_fmas_f32 v18, v18, v22, v19
	v_lshlrev_b32_e32 v19, 16, v11
	v_fma_f32 v21, -v66, v77, v19
	v_lshlrev_b32_e32 v19, 16, v15
	v_fma_f32 v22, -v66, v78, v19
	v_mul_f32_e32 v19, v22, v22
	v_lshlrev_b32_e32 v23, 16, v7
	v_fmac_f32_e32 v19, v21, v21
	v_fma_f32 v23, -v66, v76, v23
	v_fmac_f32_e32 v19, v23, v23
	v_fmac_f32_e32 v19, v24, v24
	s_nop 1
	v_mov_b32_dpp v25, v19 quad_perm:[1,0,3,2] row_mask:0xf bank_mask:0xf
	v_div_fixup_f32 v20, v18, v20, 1.0
	v_mul_f32_e32 v10, v10, v20
	v_mul_f32_e32 v10, v41, v10
	v_mul_f32_e32 v10, 0x41800000, v10
	v_cvt_pk_fp8_f32 v26, v10, v10
	s_waitcnt lgkmcnt(0)
; __device__ __forceinline__ unsigned char f2fp8(float a) { return (unsigned char)(__builtin_amdgcn_cvt_pk_fp8_f32(a, a, 0, false) & 0xff); }
; __device__ __forceinline__ float bf_lo(unsigned w) { return __uint_as_float(w << 16); }
; __device__ __forceinline__ float bf_hi(unsigned w) { return __uint_as_float(w & 0xffff0000u); }
; __device__ __forceinline__ int crow(int r, int hi) { return (r & 3) + 8 * (r >> 2) + 4 * hi; }
; __device__ __forceinline__ void p3_attention(Frame& F) {
;     ...
;         for (int r = 0; r < 16; ++r) {
;             float dd[4], ss = 0.f;
; #pragma unroll
;             for (int d = 0; d < 4; ++d) { const unsigned pw = o1p[d * 2 + (r >> 3)][(r & 7) >> 1]; const float o1 = (r & 1) ? bf_hi(pw) : bf_lo(pw); dd[d] = o1 - lam * o[d][r]; ss += dd[d] * dd[d]; }
;             ss += __shfl_xor(ss, 1); ss += __shfl_xor(ss, 2); ss += __shfl_xor(ss, 4); ss += __shfl_xor(ss, 8); ss += __shfl_xor(ss, 16);
;             const float rs = 1.0f / sqrtf(ss * (1.0f / 128.0f) + RMS_EPS);
;             unsigned char* orow = od + (size_t)attn::crow(r, hi1) * 1024;
; #pragma unroll
;             for (int d = 0; d < 4; ++d) orow[d * 32] = f2fp8(dd[d] * rs * sw[d] * OSCALE);
	v_add_f32_e32 v10, v19, v25
	s_nop 1
	v_mov_b32_dpp v25, v10 quad_perm:[2,3,0,1] row_mask:0xf bank_mask:0xf
	v_add_u32_e32 v18, 17, v36
	v_ashrrev_i32_e32 v19, 31, v18
	v_lshlrev_b64 v[18:19], 10, v[18:19]
	v_mul_f32_e32 v14, v14, v20
	s_waitcnt lgkmcnt(0)
	v_add_f32_e32 v10, v10, v25
	s_nop 1
	v_mov_b32_dpp v25, v10 row_shl:4 row_mask:0xf bank_mask:0x5
	s_nop 1
	v_mov_b32_dpp v25, v10 row_shr:4 row_mask:0xf bank_mask:0xa
	v_lshl_add_u64 v[18:19], v[34:35], 0, v[18:19]
	v_mul_f32_e32 v14, v40, v14
	global_store_byte v[18:19], v26, off
	v_mul_f32_e32 v14, 0x41800000, v14
	s_waitcnt lgkmcnt(0)
	v_add_f32_e32 v10, v10, v25
	s_nop 1
	v_mov_b32_dpp v25, v10 row_ror:8 row_mask:0xf bank_mask:0xf
	v_mov_b32_e32 v26, 0
	v_cvt_pk_fp8_f32 v26, v14, v14
	v_mul_f32_e32 v6, v6, v20
	v_mul_f32_e32 v6, v39, v6
	s_waitcnt lgkmcnt(0)
	v_add_f32_e32 v10, v10, v25
	v_mov_b32_e32 v14, v10
	s_nop 1
	v_permlane16_swap_b32_e32 v14, v10
	v_mul_f32_e32 v6, 0x41800000, v6
	v_mov_b32_e32 v25, 0
	v_cvt_pk_fp8_f32 v25, v6, v6
	v_mul_f32_e32 v2, v2, v20
	s_waitcnt lgkmcnt(0)
	v_add_f32_e32 v6, v10, v14
	v_fmamk_f32 v6, v6, 0x3c000000, v48
	v_mul_f32_e32 v10, 0x4f800000, v6
	v_cmp_gt_f32_e32 vcc, s6, v6
	v_mul_f32_e32 v2, v38, v2
	v_mul_f32_e32 v2, 0x41800000, v2
	v_cndmask_b32_e32 v6, v6, v10, vcc
	v_sqrt_f32_e32 v10, v6
	v_mov_b32_e32 v14, 0
	v_cvt_pk_fp8_f32 v14, v2, v2
	global_store_byte v[18:19], v26, off offset:32
	global_store_byte v[18:19], v25, off offset:64
	global_store_byte v[18:19], v14, off offset:96
	v_add_u32_e32 v2, -1, v10
	v_fma_f32 v20, -v2, v10, v6
	v_cmp_ge_f32_e64 s[4:5], 0, v20
	v_add_u32_e32 v20, 1, v10
	v_and_b32_e32 v11, 0xffff0000, v11
	v_cndmask_b32_e64 v2, v10, v2, s[4:5]
	v_fma_f32 v10, -v20, v10, v6
	v_cmp_lt_f32_e64 s[4:5], 0, v10
	v_fma_f32 v11, -v66, v73, v11
	v_and_b32_e32 v7, 0xffff0000, v7
	v_cndmask_b32_e64 v2, v2, v20, s[4:5]
	v_mul_f32_e32 v10, 0x37800000, v2
	v_cndmask_b32_e32 v2, v2, v10, vcc
	v_cmp_class_f32_e32 vcc, v6, v54
	v_fma_f32 v7, -v66, v72, v7
	v_mov_b32_e32 v20, 0
	v_cndmask_b32_e32 v2, v2, v6, vcc
	v_div_scale_f32 v6, s[4:5], v2, v2, 1.0
	v_rcp_f32_e32 v10, v6
	s_nop 0
	v_fma_f32 v14, -v6, v10, 1.0
	v_fmac_f32_e32 v10, v14, v10
	v_div_scale_f32 v14, vcc, 1.0, v2, 1.0
	v_mul_f32_e32 v18, v14, v10
	v_fma_f32 v19, -v6, v18, v14
	v_fmac_f32_e32 v18, v19, v10
	v_fma_f32 v6, -v6, v18, v14
	v_and_b32_e32 v14, 0xffff0000, v15
	v_fma_f32 v14, -v66, v74, v14
	v_mul_f32_e32 v15, v14, v14
	v_fmac_f32_e32 v15, v11, v11
	v_div_fmas_f32 v6, v6, v10, v18
	v_fmac_f32_e32 v15, v7, v7
	v_fma_f32 v18, -v66, v71, v3
	v_fmac_f32_e32 v15, v18, v18
	s_nop 1
	v_mov_b32_dpp v3, v15 quad_perm:[1,0,3,2] row_mask:0xf bank_mask:0xf
	v_div_fixup_f32 v6, v6, v2, 1.0
	v_mul_f32_e32 v10, v21, v6
	v_mul_f32_e32 v10, v41, v10
	v_mul_f32_e32 v10, 0x41800000, v10
	v_mov_b32_e32 v19, 0
	v_cvt_pk_fp8_f32 v19, v10, v10
	s_waitcnt lgkmcnt(0)
	v_add_f32_e32 v10, v15, v3
	s_nop 1
	v_mov_b32_dpp v15, v10 quad_perm:[2,3,0,1] row_mask:0xf bank_mask:0xf
	v_add_u32_e32 v2, 18, v36
	v_ashrrev_i32_e32 v3, 31, v2
	v_lshlrev_b64 v[2:3], 10, v[2:3]
	v_lshl_add_u64 v[2:3], v[34:35], 0, v[2:3]
	s_waitcnt lgkmcnt(0)
	v_add_f32_e32 v10, v10, v15
	s_nop 1
	v_mov_b32_dpp v15, v10 row_shl:4 row_mask:0xf bank_mask:0x5
	s_nop 1
	v_mov_b32_dpp v15, v10 row_shr:4 row_mask:0xf bank_mask:0xa
	global_store_byte v[2:3], v19, off
	v_mul_f32_e32 v19, v22, v6
	v_mul_f32_e32 v19, v40, v19
	v_mul_f32_e32 v19, 0x41800000, v19
	s_waitcnt lgkmcnt(0)
	v_add_f32_e32 v10, v10, v15
	s_nop 1
	v_mov_b32_dpp v15, v10 row_ror:8 row_mask:0xf bank_mask:0xf
	v_cvt_pk_fp8_f32 v20, v19, v19
	v_mul_f32_e32 v19, v23, v6
	v_mul_f32_e32 v19, v39, v19
	v_mul_f32_e32 v6, v24, v6
	s_waitcnt lgkmcnt(0)
	v_add_f32_e32 v10, v10, v15
	v_mov_b32_e32 v15, v10
	s_nop 1
	v_permlane16_swap_b32_e32 v15, v10
	v_mul_f32_e32 v19, 0x41800000, v19
	v_mov_b32_e32 v21, 0
	v_mul_f32_e32 v6, v38, v6
	v_cvt_pk_fp8_f32 v21, v19, v19
	s_waitcnt lgkmcnt(0)
	v_add_f32_e32 v10, v10, v15
	v_fmamk_f32 v10, v10, 0x3c000000, v48
	v_mul_f32_e32 v15, 0x4f800000, v10
	v_cmp_gt_f32_e32 vcc, s6, v10
	v_mul_f32_e32 v6, 0x41800000, v6
	v_mov_b32_e32 v19, 0
	v_cndmask_b32_e32 v10, v10, v15, vcc
	v_sqrt_f32_e32 v15, v10
	v_cvt_pk_fp8_f32 v19, v6, v6
	global_store_byte v[2:3], v20, off offset:32
	global_store_byte v[2:3], v21, off offset:64
	global_store_byte v[2:3], v19, off offset:96
	v_add_u32_e32 v6, -1, v15
	v_fma_f32 v22, -v6, v15, v10
	v_cmp_ge_f32_e64 s[4:5], 0, v22
	v_add_u32_e32 v22, 1, v15
	v_lshlrev_b32_e32 v20, 16, v4
	v_cndmask_b32_e64 v6, v15, v6, s[4:5]
	v_fma_f32 v15, -v22, v15, v10
	v_cmp_lt_f32_e64 s[4:5], 0, v15
	v_fma_f32 v20, -v66, v67, v20
	v_and_b32_e32 v4, 0xffff0000, v4
	v_cndmask_b32_e64 v6, v6, v22, s[4:5]
	v_mul_f32_e32 v15, 0x37800000, v6
	v_cndmask_b32_e32 v6, v6, v15, vcc
	v_cmp_class_f32_e32 vcc, v10, v54
	v_mov_b32_e32 v22, 0
	v_fma_f32 v4, -v66, v59, v4
	v_cndmask_b32_e32 v6, v6, v10, vcc
	v_div_scale_f32 v10, s[4:5], v6, v6, 1.0
	v_rcp_f32_e32 v15, v10
	s_nop 0
	v_fma_f32 v2, -v10, v15, 1.0
	v_fmac_f32_e32 v15, v2, v15
	v_div_scale_f32 v2, vcc, 1.0, v6, 1.0
	v_mul_f32_e32 v3, v2, v15
	v_fma_f32 v19, -v10, v3, v2
	v_fmac_f32_e32 v3, v19, v15
	v_fma_f32 v2, -v10, v3, v2
	v_div_fmas_f32 v2, v2, v15, v3
	v_div_fixup_f32 v6, v2, v6, 1.0
	v_mul_f32_e32 v3, v11, v6
	v_lshlrev_b32_e32 v11, 16, v16
	v_lshlrev_b32_e32 v10, 16, v12
	v_fma_f32 v11, -v66, v70, v11
	v_fma_f32 v10, -v66, v69, v10
	v_mul_f32_e32 v15, v11, v11
	v_lshlrev_b32_e32 v19, 16, v8
	v_fmac_f32_e32 v15, v10, v10
	v_fma_f32 v19, -v66, v68, v19
	v_fmac_f32_e32 v15, v19, v19
	v_fmac_f32_e32 v15, v20, v20
	s_nop 1
	v_mov_b32_dpp v21, v15 quad_perm:[1,0,3,2] row_mask:0xf bank_mask:0xf
	v_mul_f32_e32 v3, v41, v3
	v_mul_f32_e32 v3, 0x41800000, v3
	v_add_u32_e32 v2, 19, v36
	v_cvt_pk_fp8_f32 v22, v3, v3
	s_waitcnt lgkmcnt(0)
; __device__ __forceinline__ unsigned char f2fp8(float a) { return (unsigned char)(__builtin_amdgcn_cvt_pk_fp8_f32(a, a, 0, false) & 0xff); }
; __device__ __forceinline__ float bf_lo(unsigned w) { return __uint_as_float(w << 16); }
; __device__ __forceinline__ float bf_hi(unsigned w) { return __uint_as_float(w & 0xffff0000u); }
; __device__ __forceinline__ int crow(int r, int hi) { return (r & 3) + 8 * (r >> 2) + 4 * hi; }
; __device__ __forceinline__ void p3_attention(Frame& F) {
;     ...
;         for (int r = 0; r < 16; ++r) {
;             float dd[4], ss = 0.f;
; #pragma unroll
;             for (int d = 0; d < 4; ++d) { const unsigned pw = o1p[d * 2 + (r >> 3)][(r & 7) >> 1]; const float o1 = (r & 1) ? bf_hi(pw) : bf_lo(pw); dd[d] = o1 - lam * o[d][r]; ss += dd[d] * dd[d]; }
;             ss += __shfl_xor(ss, 1); ss += __shfl_xor(ss, 2); ss += __shfl_xor(ss, 4); ss += __shfl_xor(ss, 8); ss += __shfl_xor(ss, 16);
;             const float rs = 1.0f / sqrtf(ss * (1.0f / 128.0f) + RMS_EPS);
;             unsigned char* orow = od + (size_t)attn::crow(r, hi1) * 1024;
; #pragma unroll
;             for (int d = 0; d < 4; ++d) orow[d * 32] = f2fp8(dd[d] * rs * sw[d] * OSCALE);
	v_add_f32_e32 v15, v15, v21
	s_nop 1
	v_mov_b32_dpp v21, v15 quad_perm:[2,3,0,1] row_mask:0xf bank_mask:0xf
	v_ashrrev_i32_e32 v3, 31, v2
	v_lshlrev_b64 v[2:3], 10, v[2:3]
	v_mul_f32_e32 v14, v14, v6
	v_lshl_add_u64 v[2:3], v[34:35], 0, v[2:3]
	s_waitcnt lgkmcnt(0)
	v_add_f32_e32 v15, v15, v21
	s_nop 1
	v_mov_b32_dpp v21, v15 row_shl:4 row_mask:0xf bank_mask:0x5
	s_nop 1
	v_mov_b32_dpp v21, v15 row_shr:4 row_mask:0xf bank_mask:0xa
	v_mul_f32_e32 v14, v40, v14
	global_store_byte v[2:3], v22, off
	v_mul_f32_e32 v14, 0x41800000, v14
	v_mov_b32_e32 v22, 0
	s_waitcnt lgkmcnt(0)
	v_add_f32_e32 v15, v15, v21
	s_nop 1
	v_mov_b32_dpp v21, v15 row_ror:8 row_mask:0xf bank_mask:0xf
	v_cvt_pk_fp8_f32 v22, v14, v14
	v_mul_f32_e32 v7, v7, v6
	v_mul_f32_e32 v7, v39, v7
	v_mul_f32_e32 v7, 0x41800000, v7
	s_waitcnt lgkmcnt(0)
	v_add_f32_e32 v14, v15, v21
	v_mov_b32_e32 v15, v14
	s_nop 1
	v_permlane16_swap_b32_e32 v15, v14
	v_mov_b32_e32 v21, 0
	v_cvt_pk_fp8_f32 v21, v7, v7
	v_mul_f32_e32 v6, v18, v6
	v_mul_f32_e32 v6, v38, v6
	s_waitcnt lgkmcnt(0)
	v_add_f32_e32 v7, v14, v15
	v_fmamk_f32 v7, v7, 0x3c000000, v48
	v_mul_f32_e32 v14, 0x4f800000, v7
	v_cmp_gt_f32_e32 vcc, s6, v7
	v_mul_f32_e32 v6, 0x41800000, v6
	v_mov_b32_e32 v15, 0
	v_cndmask_b32_e32 v7, v7, v14, vcc
	v_sqrt_f32_e32 v14, v7
	v_cvt_pk_fp8_f32 v15, v6, v6
	global_store_byte v[2:3], v22, off offset:32
	global_store_byte v[2:3], v21, off offset:64
	global_store_byte v[2:3], v15, off offset:96
	v_add_u32_e32 v6, -1, v14
	v_fma_f32 v18, -v6, v14, v7
	v_cmp_ge_f32_e64 s[4:5], 0, v18
	v_add_u32_e32 v18, 1, v14
	v_and_b32_e32 v8, 0xffff0000, v8
	v_cndmask_b32_e64 v6, v14, v6, s[4:5]
	v_fma_f32 v14, -v18, v14, v7
	v_cmp_lt_f32_e64 s[4:5], 0, v14
	v_fma_f32 v8, -v66, v60, v8
	s_nop 0
	v_cndmask_b32_e64 v6, v6, v18, s[4:5]
	v_mul_f32_e32 v14, 0x37800000, v6
	v_cndmask_b32_e32 v6, v6, v14, vcc
	v_cmp_class_f32_e32 vcc, v7, v54
	s_nop 1
	v_cndmask_b32_e32 v6, v6, v7, vcc
	v_div_scale_f32 v7, s[4:5], v6, v6, 1.0
	v_rcp_f32_e32 v14, v7
	s_nop 0
	v_fma_f32 v2, -v7, v14, 1.0
	v_fmac_f32_e32 v14, v2, v14
	v_div_scale_f32 v2, vcc, 1.0, v6, 1.0
	v_mul_f32_e32 v3, v2, v14
	v_fma_f32 v15, -v7, v3, v2
	v_fmac_f32_e32 v3, v15, v14
	v_fma_f32 v2, -v7, v3, v2
	v_div_fmas_f32 v2, v2, v14, v3
	v_div_fixup_f32 v6, v2, v6, 1.0
	v_mul_f32_e32 v3, v10, v6
	v_and_b32_e32 v10, 0xffff0000, v16
	v_and_b32_e32 v7, 0xffff0000, v12
	v_fma_f32 v10, -v66, v62, v10
	v_fma_f32 v7, -v66, v61, v7
	v_mul_f32_e32 v12, v10, v10
	v_fmac_f32_e32 v12, v7, v7
	v_fmac_f32_e32 v12, v8, v8
	v_fmac_f32_e32 v12, v4, v4
	s_nop 1
	v_mov_b32_dpp v14, v12 quad_perm:[1,0,3,2] row_mask:0xf bank_mask:0xf
	v_mul_f32_e32 v3, v41, v3
	v_mul_f32_e32 v3, 0x41800000, v3
	v_mov_b32_e32 v15, 0
	v_add_u32_e32 v2, 24, v36
	s_waitcnt lgkmcnt(0)
	v_add_f32_e32 v12, v12, v14
	s_nop 1
	v_mov_b32_dpp v14, v12 quad_perm:[2,3,0,1] row_mask:0xf bank_mask:0xf
	v_cvt_pk_fp8_f32 v15, v3, v3
	v_ashrrev_i32_e32 v3, 31, v2
	v_lshlrev_b64 v[2:3], 10, v[2:3]
	v_mul_f32_e32 v11, v11, v6
	s_waitcnt lgkmcnt(0)
	v_add_f32_e32 v12, v12, v14
	s_nop 1
	v_mov_b32_dpp v14, v12 row_shl:4 row_mask:0xf bank_mask:0x5
	s_nop 1
	v_mov_b32_dpp v14, v12 row_shr:4 row_mask:0xf bank_mask:0xa
	v_lshl_add_u64 v[2:3], v[34:35], 0, v[2:3]
	v_mul_f32_e32 v11, v40, v11
	global_store_byte v[2:3], v15, off
	v_mul_f32_e32 v11, 0x41800000, v11
	s_waitcnt lgkmcnt(0)
	v_add_f32_e32 v12, v12, v14
	s_nop 1
	v_mov_b32_dpp v14, v12 row_ror:8 row_mask:0xf bank_mask:0xf
	v_mov_b32_e32 v15, 0
	v_cvt_pk_fp8_f32 v15, v11, v11
	v_mul_f32_e32 v11, v19, v6
	v_mul_f32_e32 v11, v39, v11
	s_waitcnt lgkmcnt(0)
	v_add_f32_e32 v12, v12, v14
	v_mov_b32_e32 v14, v12
	s_nop 1
	v_permlane16_swap_b32_e32 v14, v12
	v_mul_f32_e32 v11, 0x41800000, v11
	v_mov_b32_e32 v16, 0
	v_cvt_pk_fp8_f32 v16, v11, v11
	v_mul_f32_e32 v6, v20, v6
	s_waitcnt lgkmcnt(0)
	v_add_f32_e32 v11, v12, v14
	v_fmamk_f32 v11, v11, 0x3c000000, v48
	v_mul_f32_e32 v12, 0x4f800000, v11
	v_cmp_gt_f32_e32 vcc, s6, v11
	v_mul_f32_e32 v6, v38, v6
	v_mul_f32_e32 v6, 0x41800000, v6
	v_cndmask_b32_e32 v11, v11, v12, vcc
	v_sqrt_f32_e32 v12, v11
	v_mov_b32_e32 v14, 0
	v_cvt_pk_fp8_f32 v14, v6, v6
	global_store_byte v[2:3], v15, off offset:32
	global_store_byte v[2:3], v16, off offset:64
	global_store_byte v[2:3], v14, off offset:96
	v_add_u32_e32 v6, -1, v12
	v_fma_f32 v18, -v6, v12, v11
	v_cmp_ge_f32_e64 s[4:5], 0, v18
	v_add_u32_e32 v18, 1, v12
	v_lshlrev_b32_e32 v15, 16, v5
	v_cndmask_b32_e64 v6, v12, v6, s[4:5]
	v_fma_f32 v12, -v18, v12, v11
	v_cmp_lt_f32_e64 s[4:5], 0, v12
	v_fma_f32 v15, -v66, v55, v15
	v_and_b32_e32 v5, 0xffff0000, v5
	v_cndmask_b32_e64 v6, v6, v18, s[4:5]
	v_mul_f32_e32 v12, 0x37800000, v6
	v_cndmask_b32_e32 v6, v6, v12, vcc
	v_cmp_class_f32_e32 vcc, v11, v54
	v_mov_b32_e32 v18, 0
	v_fma_f32 v5, -v66, v42, v5
	v_cndmask_b32_e32 v6, v6, v11, vcc
	v_div_scale_f32 v11, s[4:5], v6, v6, 1.0
	v_rcp_f32_e32 v12, v11
	s_nop 0
	v_fma_f32 v2, -v11, v12, 1.0
	v_fmac_f32_e32 v12, v2, v12
	v_div_scale_f32 v2, vcc, 1.0, v6, 1.0
	v_mul_f32_e32 v3, v2, v12
	v_fma_f32 v14, -v11, v3, v2
	v_fmac_f32_e32 v3, v14, v12
	v_fma_f32 v2, -v11, v3, v2
	v_div_fmas_f32 v2, v2, v12, v3
	v_div_fixup_f32 v6, v2, v6, 1.0
	v_lshlrev_b32_e32 v11, 16, v17
	v_mul_f32_e32 v3, v7, v6
	v_lshlrev_b32_e32 v7, 16, v13
	v_fma_f32 v11, -v66, v58, v11
	v_fma_f32 v7, -v66, v57, v7
	v_mul_f32_e32 v12, v11, v11
	v_lshlrev_b32_e32 v14, 16, v9
	v_fmac_f32_e32 v12, v7, v7
	v_fma_f32 v14, -v66, v56, v14
	v_fmac_f32_e32 v12, v14, v14
	v_fmac_f32_e32 v12, v15, v15
	s_nop 1
	v_mov_b32_dpp v16, v12 quad_perm:[1,0,3,2] row_mask:0xf bank_mask:0xf
	v_mul_f32_e32 v3, v41, v3
	v_mul_f32_e32 v3, 0x41800000, v3
	v_add_u32_e32 v2, 25, v36
	v_cvt_pk_fp8_f32 v18, v3, v3
	s_waitcnt lgkmcnt(0)
; __device__ __forceinline__ unsigned char f2fp8(float a) { return (unsigned char)(__builtin_amdgcn_cvt_pk_fp8_f32(a, a, 0, false) & 0xff); }
; __device__ __forceinline__ float bf_lo(unsigned w) { return __uint_as_float(w << 16); }
; __device__ __forceinline__ float bf_hi(unsigned w) { return __uint_as_float(w & 0xffff0000u); }
; __device__ __forceinline__ int crow(int r, int hi) { return (r & 3) + 8 * (r >> 2) + 4 * hi; }
; __device__ __forceinline__ void p3_attention(Frame& F) {
;     ...
;         for (int r = 0; r < 16; ++r) {
;             float dd[4], ss = 0.f;
; #pragma unroll
;             for (int d = 0; d < 4; ++d) { const unsigned pw = o1p[d * 2 + (r >> 3)][(r & 7) >> 1]; const float o1 = (r & 1) ? bf_hi(pw) : bf_lo(pw); dd[d] = o1 - lam * o[d][r]; ss += dd[d] * dd[d]; }
;             ss += __shfl_xor(ss, 1); ss += __shfl_xor(ss, 2); ss += __shfl_xor(ss, 4); ss += __shfl_xor(ss, 8); ss += __shfl_xor(ss, 16);
;             const float rs = 1.0f / sqrtf(ss * (1.0f / 128.0f) + RMS_EPS);
;             unsigned char* orow = od + (size_t)attn::crow(r, hi1) * 1024;
; #pragma unroll
;             for (int d = 0; d < 4; ++d) orow[d * 32] = f2fp8(dd[d] * rs * sw[d] * OSCALE);
	v_add_f32_e32 v12, v12, v16
	s_nop 1
	v_mov_b32_dpp v16, v12 quad_perm:[2,3,0,1] row_mask:0xf bank_mask:0xf
	v_ashrrev_i32_e32 v3, 31, v2
	v_lshlrev_b64 v[2:3], 10, v[2:3]
	v_mul_f32_e32 v10, v10, v6
	v_lshl_add_u64 v[2:3], v[34:35], 0, v[2:3]
	s_waitcnt lgkmcnt(0)
	v_add_f32_e32 v12, v12, v16
	s_nop 1
	v_mov_b32_dpp v16, v12 row_shl:4 row_mask:0xf bank_mask:0x5
	s_nop 1
	v_mov_b32_dpp v16, v12 row_shr:4 row_mask:0xf bank_mask:0xa
	v_mul_f32_e32 v10, v40, v10
	global_store_byte v[2:3], v18, off
	v_mul_f32_e32 v10, 0x41800000, v10
	v_mov_b32_e32 v18, 0
	s_waitcnt lgkmcnt(0)
	v_add_f32_e32 v12, v12, v16
	s_nop 1
	v_mov_b32_dpp v16, v12 row_ror:8 row_mask:0xf bank_mask:0xf
	v_cvt_pk_fp8_f32 v18, v10, v10
	v_mul_f32_e32 v8, v8, v6
	v_mul_f32_e32 v8, v39, v8
	v_mul_f32_e32 v4, v4, v6
	s_waitcnt lgkmcnt(0)
	v_add_f32_e32 v10, v12, v16
	v_mov_b32_e32 v12, v10
	s_nop 1
	v_permlane16_swap_b32_e32 v12, v10
	v_mul_f32_e32 v8, 0x41800000, v8
	v_mov_b32_e32 v16, 0
	v_cvt_pk_fp8_f32 v16, v8, v8
	v_mul_f32_e32 v4, v38, v4
	s_waitcnt lgkmcnt(0)
	v_add_f32_e32 v6, v10, v12
	v_fmamk_f32 v6, v6, 0x3c000000, v48
	v_mul_f32_e32 v8, 0x4f800000, v6
	v_cmp_gt_f32_e32 vcc, s6, v6
	v_mul_f32_e32 v4, 0x41800000, v4
	v_mov_b32_e32 v10, 0
	v_cndmask_b32_e32 v6, v6, v8, vcc
	v_sqrt_f32_e32 v8, v6
	v_cvt_pk_fp8_f32 v10, v4, v4
	global_store_byte v[2:3], v18, off offset:32
	global_store_byte v[2:3], v16, off offset:64
	global_store_byte v[2:3], v10, off offset:96
	v_add_u32_e32 v4, -1, v8
	v_fma_f32 v12, -v4, v8, v6
	v_cmp_ge_f32_e64 s[4:5], 0, v12
	v_add_u32_e32 v12, 1, v8
	v_and_b32_e32 v9, 0xffff0000, v9
	v_cndmask_b32_e64 v4, v8, v4, s[4:5]
	v_fma_f32 v8, -v12, v8, v6
	v_cmp_lt_f32_e64 s[4:5], 0, v8
	v_fma_f32 v9, -v66, v43, v9
	s_nop 0
	v_cndmask_b32_e64 v4, v4, v12, s[4:5]
	v_mul_f32_e32 v8, 0x37800000, v4
	v_cndmask_b32_e32 v4, v4, v8, vcc
	v_cmp_class_f32_e32 vcc, v6, v54
	v_mov_b32_e32 v12, 0
	s_nop 0
	v_cndmask_b32_e32 v4, v4, v6, vcc
	v_div_scale_f32 v6, s[4:5], v4, v4, 1.0
	v_rcp_f32_e32 v8, v6
	s_nop 0
	v_fma_f32 v2, -v6, v8, 1.0
	v_fmac_f32_e32 v8, v2, v8
	v_div_scale_f32 v2, vcc, 1.0, v4, 1.0
	v_mul_f32_e32 v3, v2, v8
	v_fma_f32 v10, -v6, v3, v2
	v_fmac_f32_e32 v3, v10, v8
	v_fma_f32 v2, -v6, v3, v2
	v_div_fmas_f32 v2, v2, v8, v3
	v_div_fixup_f32 v4, v2, v4, 1.0
	v_mul_f32_e32 v3, v7, v4
	v_and_b32_e32 v7, 0xffff0000, v17
	v_and_b32_e32 v6, 0xffff0000, v13
	v_fma_f32 v7, -v66, v44, v7
	v_fma_f32 v6, -v66, v45, v6
	v_mul_f32_e32 v8, v7, v7
	v_fmac_f32_e32 v8, v6, v6
	v_fmac_f32_e32 v8, v9, v9
	v_fmac_f32_e32 v8, v5, v5
	s_nop 1
	v_mov_b32_dpp v10, v8 quad_perm:[1,0,3,2] row_mask:0xf bank_mask:0xf
	v_mul_f32_e32 v3, v41, v3
	v_mul_f32_e32 v3, 0x41800000, v3
	v_add_u32_e32 v2, 26, v36
	v_cvt_pk_fp8_f32 v12, v3, v3
	s_waitcnt lgkmcnt(0)
	v_add_f32_e32 v8, v8, v10
	s_nop 1
	v_mov_b32_dpp v10, v8 quad_perm:[2,3,0,1] row_mask:0xf bank_mask:0xf
	v_ashrrev_i32_e32 v3, 31, v2
	v_lshlrev_b64 v[2:3], 10, v[2:3]
	v_mul_f32_e32 v11, v11, v4
	v_lshl_add_u64 v[2:3], v[34:35], 0, v[2:3]
	s_waitcnt lgkmcnt(0)
	v_add_f32_e32 v8, v8, v10
	s_nop 1
	v_mov_b32_dpp v10, v8 row_shl:4 row_mask:0xf bank_mask:0x5
	s_nop 1
	v_mov_b32_dpp v10, v8 row_shr:4 row_mask:0xf bank_mask:0xa
	v_mul_f32_e32 v11, v40, v11
	global_store_byte v[2:3], v12, off
	v_mul_f32_e32 v11, 0x41800000, v11
	v_mov_b32_e32 v12, 0
	s_waitcnt lgkmcnt(0)
	v_add_f32_e32 v8, v8, v10
	s_nop 1
	v_mov_b32_dpp v10, v8 row_ror:8 row_mask:0xf bank_mask:0xf
	v_cvt_pk_fp8_f32 v12, v11, v11
	v_mul_f32_e32 v11, v14, v4
	v_mul_f32_e32 v11, v39, v11
	v_mul_f32_e32 v4, v15, v4
	s_waitcnt lgkmcnt(0)
	v_add_f32_e32 v8, v8, v10
	v_mov_b32_e32 v10, v8
	s_nop 1
	v_permlane16_swap_b32_e32 v10, v8
	v_mul_f32_e32 v11, 0x41800000, v11
	v_mov_b32_e32 v13, 0
	v_mul_f32_e32 v4, v38, v4
	v_cvt_pk_fp8_f32 v13, v11, v11
	s_waitcnt lgkmcnt(0)
	v_add_f32_e32 v8, v8, v10
	v_fmac_f32_e32 v48, 0x3c000000, v8
	v_mul_f32_e32 v8, 0x4f800000, v48
	v_cmp_gt_f32_e32 vcc, s6, v48
	v_mul_f32_e32 v4, 0x41800000, v4
	v_mov_b32_e32 v11, 0
	v_cndmask_b32_e32 v8, v48, v8, vcc
	v_sqrt_f32_e32 v10, v8
	v_cvt_pk_fp8_f32 v11, v4, v4
	global_store_byte v[2:3], v12, off offset:32
	global_store_byte v[2:3], v13, off offset:64
	global_store_byte v[2:3], v11, off offset:96
	v_add_u32_e32 v4, -1, v10
	v_fma_f32 v14, -v4, v10, v8
	v_cmp_ge_f32_e64 s[4:5], 0, v14
	v_add_u32_e32 v14, 1, v10
	s_nop 0
	v_cndmask_b32_e64 v4, v10, v4, s[4:5]
	v_fma_f32 v10, -v14, v10, v8
	v_cmp_lt_f32_e64 s[4:5], 0, v10
	s_nop 1
	v_cndmask_b32_e64 v4, v4, v14, s[4:5]
	v_mul_f32_e32 v10, 0x37800000, v4
	v_cndmask_b32_e32 v4, v4, v10, vcc
	v_cmp_class_f32_e32 vcc, v8, v54
	s_nop 1
	v_cndmask_b32_e32 v4, v4, v8, vcc
	v_div_scale_f32 v8, s[4:5], v4, v4, 1.0
	v_rcp_f32_e32 v10, v8
	s_mov_b64 s[4:5], -1
	v_fma_f32 v2, -v8, v10, 1.0
	v_fmac_f32_e32 v10, v2, v10
	v_div_scale_f32 v2, vcc, 1.0, v4, 1.0
	v_mul_f32_e32 v3, v2, v10
	v_fma_f32 v11, -v8, v3, v2
	v_fmac_f32_e32 v3, v11, v10
	v_fma_f32 v2, -v8, v3, v2
	v_div_fmas_f32 v2, v2, v10, v3
	v_div_fixup_f32 v4, v2, v4, 1.0
	v_mul_f32_e32 v6, v6, v4
	v_mul_f32_e32 v6, v41, v6
	v_mul_f32_e32 v6, 0x41800000, v6
	v_mov_b32_e32 v8, 0
	v_cvt_pk_fp8_f32 v8, v6, v6
	v_mul_f32_e32 v6, v7, v4
	v_mul_f32_e32 v6, v40, v6
	v_mul_f32_e32 v6, 0x41800000, v6
	v_mov_b32_e32 v7, 0
	v_cvt_pk_fp8_f32 v7, v6, v6
	v_mul_f32_e32 v6, v9, v4
	v_add_u32_e32 v2, 27, v36
	v_mul_f32_e32 v6, v39, v6
	v_mul_f32_e32 v4, v5, v4
	v_ashrrev_i32_e32 v3, 31, v2
	v_mul_f32_e32 v6, 0x41800000, v6
	v_mov_b32_e32 v9, 0
	v_mul_f32_e32 v4, v38, v4
	v_lshlrev_b64 v[2:3], 10, v[2:3]
	v_cvt_pk_fp8_f32 v9, v6, v6
	v_mul_f32_e32 v4, 0x41800000, v4
	v_lshl_add_u64 v[2:3], v[34:35], 0, v[2:3]
	v_cvt_pk_fp8_f32 v46, v4, v4
	global_store_byte v[2:3], v8, off
	global_store_byte v[2:3], v7, off offset:32
	global_store_byte v[2:3], v9, off offset:64
	global_store_byte v[2:3], v46, off offset:96
	s_cbranch_scc0 .LBB0_452
	s_lshl_b32 s21, s55, 2
	s_mov_b32 s57, 52
	s_cbranch_execz .LBB0_453
